# phase-B address setup hoisted into wait shadow; loop v_add pairs as v_pk_add_f32; last-block MMA with pre-loaded bank fragments
# speedup vs baseline: 1.0072x; 1.0072x over previous
_Z12fused_kernelPKfS0_Pf:
	s_load_dwordx4 s[12:15], s[0:1], 0x0
	s_load_dwordx2 s[8:9], s[0:1], 0x10
	s_lshl_b32 s0, s2, 5
	s_and_b32 s0, s0, 0xe0
	s_lshr_b32 s3, s2, 3
	s_add_i32 s0, s0, s3
	v_and_b32_e32 v1, 63, v0
	v_lshrrev_b32_e32 v200, 6, v0
	s_lshl_b32 s0, s0, 17
	v_lshlrev_b32_e32 v194, 4, v0
	v_lshl_add_u32 v2, v200, 25, s0
	v_lshlrev_b32_e32 v198, 4, v1
	v_add_u32_e32 v106, 0x2000, v194
	v_add_u32_e32 v107, 0x4000, v194
	v_or_b32_e32 v203, v2, v198
	v_lshlrev_b32_e32 v196, 10, v200
	v_mov_b32_e32 v195, 0
	v_or_b32_e32 v233, v203, v196
	s_mov_b32 s7, 0x20000
	s_brev_b32 s6, 8
	s_waitcnt lgkmcnt(0)
	s_and_b32 s5, s13, 0xffff
	s_mov_b32 s4, s12
	buffer_load_dwordx4 v[70:73], v233, s[4:7], 0 offen nt
	v_or_b32_e32 v227, 0x2000, v233
	buffer_load_dwordx4 v[66:69], v227, s[4:7], 0 offen nt
	v_or_b32_e32 v226, 0x4000, v233
	buffer_load_dwordx4 v[78:81], v226, s[4:7], 0 offen nt
	v_or_b32_e32 v227, 0x6000, v233
	buffer_load_dwordx4 v[74:77], v227, s[4:7], 0 offen nt
	v_or_b32_e32 v226, 0x8000, v233
	buffer_load_dwordx4 v[86:89], v226, s[4:7], 0 offen nt
	v_or_b32_e32 v227, 0xa000, v233
	buffer_load_dwordx4 v[82:85], v227, s[4:7], 0 offen nt
	v_or_b32_e32 v226, 0xc000, v233
	buffer_load_dwordx4 v[94:97], v226, s[4:7], 0 offen nt
	v_or_b32_e32 v227, 0xe000, v233
	buffer_load_dwordx4 v[90:93], v227, s[4:7], 0 offen nt
	v_or_b32_e32 v226, 0x10000, v233
	buffer_load_dwordx4 v[150:153], v226, s[4:7], 0 offen nt
	v_or_b32_e32 v227, 0x12000, v233
	buffer_load_dwordx4 v[146:149], v227, s[4:7], 0 offen nt
	v_or_b32_e32 v226, 0x14000, v233
	buffer_load_dwordx4 v[162:165], v226, s[4:7], 0 offen nt
	v_or_b32_e32 v227, 0x16000, v233
	buffer_load_dwordx4 v[154:157], v227, s[4:7], 0 offen nt
	v_or_b32_e32 v226, 0x18000, v233
	buffer_load_dwordx4 v[174:177], v226, s[4:7], 0 offen nt
	v_or_b32_e32 v227, 0x1a000, v233
	buffer_load_dwordx4 v[166:169], v227, s[4:7], 0 offen nt
	v_or_b32_e32 v226, 0x1c000, v233
	buffer_load_dwordx4 v[182:185], v226, s[4:7], 0 offen nt
	v_or_b32_e32 v227, 0x1e000, v233
	buffer_load_dwordx4 v[178:181], v227, s[4:7], 0 offen nt
	global_load_dwordx4 v[228:231], v194, s[14:15]
	global_load_dwordx4 v[98:101], v106, s[14:15]
	global_load_dwordx4 v[102:105], v107, s[14:15]
	v_add_u32_e32 v107, 0x6000, v194
	global_load_dwordx4 v[116:119], v107, s[14:15]
	v_add_u32_e32 v106, 0x8000, v194
	global_load_dwordx4 v[120:123], v106, s[14:15]
	v_add_u32_e32 v107, 0xa000, v194
	global_load_dwordx4 v[124:127], v107, s[14:15]
	v_add_u32_e32 v106, 0xc000, v194
	global_load_dwordx4 v[128:131], v106, s[14:15]
	v_add_u32_e32 v107, 0xe000, v194
	global_load_dwordx4 v[132:135], v107, s[14:15]
	v_add_u32_e32 v106, 0x10000, v194
	global_load_dwordx4 v[136:139], v106, s[14:15]
	v_add_u32_e32 v107, 0x12000, v194
	global_load_dwordx4 v[140:143], v107, s[14:15]
	v_add_u32_e32 v106, 0x14000, v194
	global_load_dwordx4 v[158:161], v106, s[14:15]
	v_add_u32_e32 v107, 0x16000, v194
	global_load_dwordx4 v[170:173], v107, s[14:15]
	v_add_u32_e32 v106, 0x18000, v194
	global_load_dwordx4 v[186:189], v106, s[14:15]
	v_add_u32_e32 v107, 0x1a000, v194
	global_load_dwordx4 v[190:193], v107, s[14:15]
	v_add_u32_e32 v106, 0x1c000, v194
	global_load_dwordx4 v[204:207], v106, s[14:15]
	v_add_u32_e32 v107, 0x1e000, v194
	global_load_dwordx4 v[208:211], v107, s[14:15]
	v_add_u32_e32 v106, 0x20000, v194
	global_load_dwordx4 v[212:215], v106, s[14:15]
	v_add_u32_e32 v107, 0x22000, v194
	global_load_dwordx4 v[216:219], v107, s[14:15]
	v_add_u32_e32 v106, 0x24000, v194
	global_load_dwordx4 v[220:223], v106, s[14:15]
	v_add_u32_e32 v107, 0x26000, v194
	global_load_dwordx4 v[112:115], v107, s[14:15]
	v_add_u32_e32 v224, 0x400, v196
	s_movk_i32 s0, 0x1c00
	v_and_or_b32 v224, v224, s0, v203
	buffer_load_dwordx4 v[62:65], v224, s[4:7], 0 offen nt
	v_or_b32_e32 v227, 0x2000, v224
	buffer_load_dwordx4 v[38:41], v227, s[4:7], 0 offen nt
	v_or_b32_e32 v226, 0x4000, v224
	buffer_load_dwordx4 v[42:45], v226, s[4:7], 0 offen nt
	v_or_b32_e32 v227, 0x6000, v224
	buffer_load_dwordx4 v[14:17], v227, s[4:7], 0 offen nt
	v_or_b32_e32 v226, 0x8000, v224
	buffer_load_dwordx4 v[46:49], v226, s[4:7], 0 offen nt
	v_or_b32_e32 v227, 0xa000, v224
	buffer_load_dwordx4 v[18:21], v227, s[4:7], 0 offen nt
	v_or_b32_e32 v226, 0xc000, v224
	buffer_load_dwordx4 v[50:53], v226, s[4:7], 0 offen nt
	v_or_b32_e32 v227, 0xe000, v224
	buffer_load_dwordx4 v[22:25], v227, s[4:7], 0 offen nt
	v_or_b32_e32 v226, 0x10000, v224
	buffer_load_dwordx4 v[54:57], v226, s[4:7], 0 offen nt
	v_or_b32_e32 v227, 0x12000, v224
	buffer_load_dwordx4 v[26:29], v227, s[4:7], 0 offen nt
	v_or_b32_e32 v226, 0x14000, v224
	buffer_load_dwordx4 v[58:61], v226, s[4:7], 0 offen nt
	v_or_b32_e32 v227, 0x16000, v224
	buffer_load_dwordx4 v[30:33], v227, s[4:7], 0 offen nt
	v_or_b32_e32 v226, 0x18000, v224
	buffer_load_dwordx4 v[34:37], v226, s[4:7], 0 offen nt
	v_or_b32_e32 v227, 0x1a000, v224
	buffer_load_dwordx4 v[6:9], v227, s[4:7], 0 offen nt
	v_or_b32_e32 v226, 0x1c000, v224
	buffer_load_dwordx4 v[10:13], v226, s[4:7], 0 offen nt
	v_or_b32_e32 v227, 0x1e000, v224
	buffer_load_dwordx4 v[2:5], v227, s[4:7], 0 offen nt
	s_mov_b32 s1, 0xe000
	s_mov_b32 s10, 0xa000
	s_mov_b32 s11, 0x6000
	s_mov_b32 s12, 0xc000
	s_mov_b32 s13, 0x8000
	s_mov_b32 s14, 0x1e000
	s_mov_b32 s15, 0x1c000
	s_mov_b32 s16, 0x2000
	s_mov_b32 s17, 0x4000
	s_mov_b32 s18, 0x10000
	s_mov_b32 s19, 0x1a000
	s_mov_b32 s20, 0x18000
	s_mov_b32 s21, 0x16000
	s_mov_b32 s22, 0x14000
	s_mov_b32 s23, 0x12000
	s_mov_b32 s24, 0xe0
	s_mov_b32 s26, 0x3e13bb63
	v_lshrrev_b32_e32 v144, 3, v0
	v_bfe_u32 v145, v0, 1, 2
	v_lshlrev_b32_e32 v108, 3, v0
	v_and_b32_e32 v109, 8, v108
	v_lshlrev_b32_e32 v224, 8, v144
	v_lshlrev_b32_e32 v225, 6, v145
	v_lshlrev_b32_e32 v226, 8, v145
	v_lshlrev_b32_e32 v110, 10, v144
	v_or3_b32 v110, v226, v110, v109
	v_or3_b32 v111, v224, v225, v109
	v_add_u32_e32 v111, 0xff00, v111
	v_add_u32_e32 v144, 0x24800, v194
	v_bfe_u32 v201, v0, 4, 2
	v_and_b32_e32 v197, 15, v0
	v_lshlrev_b32_e32 v202, 2, v201
	s_waitcnt vmcnt(34)
	v_pk_add_f32 v[224:225], v[228:229], 0 op_sel_hi:[1,0]
	v_pk_add_f32 v[226:227], v[230:231], 0 op_sel_hi:[1,0]
	v_cvt_pk_bf16_f32 v228, v228, v229
	v_cvt_pk_bf16_f32 v229, v230, v231
	v_pk_add_f32 v[224:225], v[224:225], v[98:99]
	v_pk_add_f32 v[226:227], v[226:227], v[100:101]
	v_cvt_pk_bf16_f32 v98, v98, v99
	v_cvt_pk_bf16_f32 v99, v100, v101
	ds_write2_b64 v110, v[228:229], v[98:99] offset1:2
	s_waitcnt vmcnt(32)
	v_pk_add_f32 v[224:225], v[224:225], v[102:103]
	v_pk_add_f32 v[226:227], v[226:227], v[104:105]
	v_cvt_pk_bf16_f32 v102, v102, v103
	v_cvt_pk_bf16_f32 v103, v104, v105
	v_pk_add_f32 v[224:225], v[224:225], v[116:117]
	v_pk_add_f32 v[226:227], v[226:227], v[118:119]
	v_cvt_pk_bf16_f32 v116, v116, v117
	v_cvt_pk_bf16_f32 v117, v118, v119
	ds_write2_b64 v110, v[102:103], v[116:117] offset0:4 offset1:6
	s_waitcnt vmcnt(30)
	v_pk_add_f32 v[224:225], v[224:225], v[120:121]
	v_pk_add_f32 v[226:227], v[226:227], v[122:123]
	v_cvt_pk_bf16_f32 v120, v120, v121
	v_cvt_pk_bf16_f32 v121, v122, v123
	v_pk_add_f32 v[224:225], v[224:225], v[124:125]
	v_pk_add_f32 v[226:227], v[226:227], v[126:127]
	v_cvt_pk_bf16_f32 v124, v124, v125
	v_cvt_pk_bf16_f32 v125, v126, v127
	ds_write2_b64 v110, v[120:121], v[124:125] offset0:8 offset1:10
	s_waitcnt vmcnt(28)
	v_pk_add_f32 v[224:225], v[224:225], v[128:129]
	v_pk_add_f32 v[226:227], v[226:227], v[130:131]
	v_cvt_pk_bf16_f32 v128, v128, v129
	v_cvt_pk_bf16_f32 v129, v130, v131
	v_pk_add_f32 v[224:225], v[224:225], v[132:133]
	v_pk_add_f32 v[226:227], v[226:227], v[134:135]
	v_cvt_pk_bf16_f32 v132, v132, v133
	v_cvt_pk_bf16_f32 v133, v134, v135
	ds_write2_b64 v110, v[128:129], v[132:133] offset0:12 offset1:14
	s_waitcnt vmcnt(26)
	v_pk_add_f32 v[224:225], v[224:225], v[136:137]
	v_pk_add_f32 v[226:227], v[226:227], v[138:139]
	v_cvt_pk_bf16_f32 v136, v136, v137
	v_cvt_pk_bf16_f32 v137, v138, v139
	v_pk_add_f32 v[224:225], v[224:225], v[140:141]
	v_pk_add_f32 v[226:227], v[226:227], v[142:143]
	v_cvt_pk_bf16_f32 v140, v140, v141
	v_cvt_pk_bf16_f32 v141, v142, v143
	ds_write2_b64 v110, v[136:137], v[140:141] offset0:16 offset1:18
	s_waitcnt vmcnt(24)
	v_pk_add_f32 v[224:225], v[224:225], v[158:159]
	v_pk_add_f32 v[226:227], v[226:227], v[160:161]
	v_cvt_pk_bf16_f32 v158, v158, v159
	v_cvt_pk_bf16_f32 v159, v160, v161
	v_pk_add_f32 v[224:225], v[224:225], v[170:171]
	v_pk_add_f32 v[226:227], v[226:227], v[172:173]
	v_cvt_pk_bf16_f32 v170, v170, v171
	v_cvt_pk_bf16_f32 v171, v172, v173
	ds_write2_b64 v110, v[158:159], v[170:171] offset0:20 offset1:22
	s_waitcnt vmcnt(22)
	v_pk_add_f32 v[224:225], v[224:225], v[186:187]
	v_pk_add_f32 v[226:227], v[226:227], v[188:189]
	v_cvt_pk_bf16_f32 v186, v186, v187
	v_cvt_pk_bf16_f32 v187, v188, v189
	v_pk_add_f32 v[224:225], v[224:225], v[190:191]
	v_pk_add_f32 v[226:227], v[226:227], v[192:193]
	v_cvt_pk_bf16_f32 v190, v190, v191
	v_cvt_pk_bf16_f32 v191, v192, v193
	ds_write2_b64 v110, v[186:187], v[190:191] offset0:24 offset1:26
	s_waitcnt vmcnt(20)
	v_pk_add_f32 v[224:225], v[224:225], v[204:205]
	v_pk_add_f32 v[226:227], v[226:227], v[206:207]
	v_cvt_pk_bf16_f32 v204, v204, v205
	v_cvt_pk_bf16_f32 v205, v206, v207
	v_pk_add_f32 v[224:225], v[224:225], v[208:209]
	v_pk_add_f32 v[226:227], v[226:227], v[210:211]
	v_cvt_pk_bf16_f32 v208, v208, v209
	v_cvt_pk_bf16_f32 v209, v210, v211
	ds_write2_b64 v110, v[204:205], v[208:209] offset0:28 offset1:30
	s_waitcnt vmcnt(18)
	v_pk_add_f32 v[224:225], v[224:225], v[212:213]
	v_pk_add_f32 v[226:227], v[226:227], v[214:215]
	v_cvt_pk_bf16_f32 v212, v212, v213
	v_cvt_pk_bf16_f32 v213, v214, v215
	v_pk_add_f32 v[224:225], v[224:225], v[216:217]
	v_pk_add_f32 v[226:227], v[226:227], v[218:219]
	v_cvt_pk_bf16_f32 v216, v216, v217
	v_cvt_pk_bf16_f32 v217, v218, v219
	ds_write2_b64 v111, v[212:213], v[216:217] offset0:32 offset1:34
	s_waitcnt vmcnt(16)
	v_pk_add_f32 v[224:225], v[224:225], v[220:221]
	v_pk_add_f32 v[226:227], v[226:227], v[222:223]
	v_cvt_pk_bf16_f32 v220, v220, v221
	v_cvt_pk_bf16_f32 v221, v222, v223
	v_pk_add_f32 v[224:225], v[224:225], v[112:113]
	v_pk_add_f32 v[226:227], v[226:227], v[114:115]
	v_cvt_pk_bf16_f32 v112, v112, v113
	v_cvt_pk_bf16_f32 v113, v114, v115
	ds_write2_b64 v111, v[220:221], v[112:113] offset0:36 offset1:38
	v_pk_mul_f32 v[224:225], v[224:225], s[26:27] op_sel_hi:[1,0]
	v_pk_mul_f32 v[226:227], v[226:227], s[26:27] op_sel_hi:[1,0]
	ds_write_b128 v144, v[224:227]
	v_and_or_b32 v98, v0, 3, v202
	v_mov_b32_e32 v99, 0x10000
	v_lshl_or_b32 v204, v98, 4, v99
	s_movk_i32 s25, 0x2100
	v_mov_b32_e32 v98, 0x14000
	v_mad_u32_u24 v199, v200, s25, v98
	v_add_u32_e32 v98, 0x800, v196
	v_and_or_b32 v186, v98, s0, v203
	v_or_b32_e32 v98, 0x2000, v186
	s_waitcnt lgkmcnt(0)
	s_barrier
	buffer_load_dwordx4 v[102:105], v186, s[4:7], 0 offen nt
	s_nop 0
	buffer_load_dwordx4 v[98:101], v98, s[4:7], 0 offen nt
	v_or_b32_e32 v106, 0x4000, v186
	v_or_b32_e32 v107, 0x6000, v186
	v_or_b32_e32 v114, 0x8000, v186
	v_or_b32_e32 v115, 0xa000, v186
	v_or_b32_e32 v122, 0xc000, v186
	v_or_b32_e32 v123, 0xe000, v186
	v_or_b32_e32 v130, 0x10000, v186
	v_or_b32_e32 v131, 0x12000, v186
	v_or_b32_e32 v138, 0x14000, v186
	v_or_b32_e32 v139, 0x16000, v186
	v_or_b32_e32 v158, 0x18000, v186
	v_or_b32_e32 v159, 0x1a000, v186
	v_or_b32_e32 v187, 0x1c000, v186
	v_or_b32_e32 v186, 0x1e000, v186
	v_or_b32_e32 v213, v199, v109
	v_and_b32_e32 v214, 0x1f0, v108
	buffer_load_dwordx4 v[110:113], v106, s[4:7], 0 offen nt
	s_nop 0
	buffer_load_dwordx4 v[106:109], v107, s[4:7], 0 offen nt
	s_nop 0
	buffer_load_dwordx4 v[118:121], v114, s[4:7], 0 offen nt
	s_nop 0
	buffer_load_dwordx4 v[114:117], v115, s[4:7], 0 offen nt
	s_nop 0
	buffer_load_dwordx4 v[126:129], v122, s[4:7], 0 offen nt
	s_nop 0
	buffer_load_dwordx4 v[122:125], v123, s[4:7], 0 offen nt
	s_nop 0
	buffer_load_dwordx4 v[134:137], v130, s[4:7], 0 offen nt
	s_nop 0
	buffer_load_dwordx4 v[130:133], v131, s[4:7], 0 offen nt
	s_nop 0
	buffer_load_dwordx4 v[142:145], v138, s[4:7], 0 offen nt
	s_nop 0
	buffer_load_dwordx4 v[138:141], v139, s[4:7], 0 offen nt
	s_nop 0
	buffer_load_dwordx4 v[170:173], v158, s[4:7], 0 offen nt
	s_nop 0
	buffer_load_dwordx4 v[158:161], v159, s[4:7], 0 offen nt
	s_nop 0
	buffer_load_dwordx4 v[190:193], v187, s[4:7], 0 offen nt
	s_nop 0
	buffer_load_dwordx4 v[186:189], v186, s[4:7], 0 offen nt
	s_waitcnt vmcnt(32)
	v_cvt_pk_bf16_f32 v66, v66, v67
	v_cvt_pk_bf16_f32 v67, v68, v69
	s_movk_i32 s25, 0x50
	v_xad_u32 v207, v214, s25, v213
	s_movk_i32 s25, 0x60
	v_xad_u32 v206, v214, s25, v213
	s_movk_i32 s25, 0x70
	v_xad_u32 v205, v214, s25, v213
	s_movk_i32 s25, 0x80
	v_xad_u32 v211, v214, 16, v213
	v_xad_u32 v231, v214, s25, v213
	s_movk_i32 s25, 0x90
	v_xad_u32 v210, v214, 32, v213
	v_xad_u32 v230, v214, s25, v213
	s_movk_i32 s25, 0xa0
	ds_write_b64 v211, v[66:67] offset:512
	v_cvt_pk_bf16_f32 v66, v78, v79
	v_cvt_pk_bf16_f32 v67, v80, v81
	v_xad_u32 v209, v214, 48, v213
	v_xad_u32 v229, v214, s25, v213
	s_movk_i32 s25, 0xb0
	ds_write_b64 v210, v[66:67] offset:1024
	v_cvt_pk_bf16_f32 v66, v74, v75
	v_cvt_pk_bf16_f32 v67, v76, v77
	v_xad_u32 v208, v214, 64, v213
	v_xad_u32 v228, v214, s25, v213
	s_movk_i32 s25, 0xc0
	ds_write_b64 v209, v[66:67] offset:1536
	v_cvt_pk_bf16_f32 v66, v86, v87
	v_cvt_pk_bf16_f32 v67, v88, v89
	v_xad_u32 v227, v214, s25, v213
	s_movk_i32 s25, 0xd0
	v_xad_u32 v225, v214, s24, v213
	s_movk_i32 s24, 0xf0
	ds_write_b64 v208, v[66:67] offset:2048
	v_cvt_pk_bf16_f32 v66, v82, v83
	v_cvt_pk_bf16_f32 v67, v84, v85
	v_add_u32_e32 v212, v213, v214
	v_xad_u32 v226, v214, s25, v213
	v_xad_u32 v224, v214, s24, v213
	v_lshl_add_u32 v213, v197, 9, v199
	v_bitop3_b32 v214, v201, v0, 15 bitop3:0x78
	ds_write_b64 v207, v[66:67] offset:2560
	v_cvt_pk_bf16_f32 v66, v94, v95
	v_cvt_pk_bf16_f32 v67, v96, v97
	v_lshl_or_b32 v223, v214, 4, v213
	v_bitop3_b32 v214, v201, v197, 4 bitop3:0x36
	ds_write_b64 v206, v[66:67] offset:3072
	v_cvt_pk_bf16_f32 v66, v90, v91
	v_cvt_pk_bf16_f32 v67, v92, v93
	v_lshl_or_b32 v222, v214, 4, v213
	v_bitop3_b32 v214, v201, v197, 8 bitop3:0x36
	ds_write_b64 v205, v[66:67] offset:3584
	v_cvt_pk_bf16_f32 v66, v150, v151
	v_cvt_pk_bf16_f32 v67, v152, v153
	v_lshl_or_b32 v221, v214, 4, v213
	v_bitop3_b32 v214, v201, v197, 12 bitop3:0x36
	ds_write_b64 v231, v[66:67] offset:4096
	v_cvt_pk_bf16_f32 v66, v146, v147
	v_cvt_pk_bf16_f32 v67, v148, v149
	v_lshl_or_b32 v219, v214, 4, v213
	v_bitop3_b32 v214, v201, v197, 16 bitop3:0x36
	ds_write_b64 v230, v[66:67] offset:4608
	v_cvt_pk_bf16_f32 v66, v162, v163
	v_cvt_pk_bf16_f32 v67, v164, v165
	v_lshl_add_u32 v218, v214, 4, v213
	v_bitop3_b32 v214, v201, v197, 20 bitop3:0x36
	ds_write_b64 v229, v[66:67] offset:5120
	v_cvt_pk_bf16_f32 v66, v154, v155
	v_cvt_pk_bf16_f32 v67, v156, v157
	v_lshl_add_u32 v217, v214, 4, v213
	v_bitop3_b32 v214, v201, v197, 24 bitop3:0x36
	ds_write_b64 v228, v[66:67] offset:5632
	v_cvt_pk_bf16_f32 v66, v174, v175
	v_cvt_pk_bf16_f32 v67, v176, v177
	v_lshl_add_u32 v216, v214, 4, v213
	v_bitop3_b32 v214, v201, v197, 28 bitop3:0x36
	ds_write_b64 v227, v[66:67] offset:6144
	v_cvt_pk_bf16_f32 v66, v166, v167
	v_cvt_pk_bf16_f32 v67, v168, v169
	v_add_u32_e32 v235, 3, v200
	v_lshl_add_u32 v213, v214, 4, v213
	ds_write_b64 v226, v[66:67] offset:6656
	v_cvt_pk_bf16_f32 v66, v182, v183
	v_cvt_pk_bf16_f32 v67, v184, v185
	v_cvt_pk_bf16_f32 v70, v70, v71
	v_cvt_pk_bf16_f32 v71, v72, v73
	ds_write_b64 v212, v[70:71]
	ds_write_b64 v225, v[66:67] offset:7168
	v_cvt_pk_bf16_f32 v66, v178, v179
	v_cvt_pk_bf16_f32 v67, v180, v181
	ds_write_b64 v224, v[66:67] offset:7680
	v_lshl_or_b32 v66, v200, 13, v198
	ds_read_b128 v[66:69], v66
	v_lshlrev_b32_e32 v220, 11, v200
	v_or_b32_e32 v70, v204, v220
	ds_read_b128 v[70:73], v70
	ds_read_b128 v[74:77], v223
	v_lshlrev_b32_e32 v232, 3, v200
	v_or_b32_e32 v214, 1, v232
	s_waitcnt lgkmcnt(0)
	v_mfma_f32_16x16x32_bf16 v[70:73], v[70:73], v[74:77], 0
	v_lshlrev_b32_e32 v215, 8, v214
	v_or_b32_e32 v78, v204, v215
	v_or_b32_e32 v184, 2, v232
	v_mfma_f32_16x16x32_bf16 v[66:69], v[66:69], v[74:77], 0
	v_lshl_or_b32 v74, v214, 10, v198
	ds_read_b128 v[74:77], v74
	ds_read_b128 v[78:81], v78
	ds_read_b128 v[82:85], v222
	v_lshlrev_b32_e32 v185, 8, v184
	s_waitcnt lgkmcnt(0)
	v_mfma_f32_16x16x32_bf16 v[70:73], v[78:81], v[82:85], v[70:73]
	v_or_b32_e32 v78, v204, v185
	v_or_b32_e32 v182, 3, v232
	v_lshlrev_b32_e32 v183, 8, v182
	v_mfma_f32_16x16x32_bf16 v[66:69], v[74:77], v[82:85], v[66:69]
	v_lshl_or_b32 v74, v184, 10, v198
	ds_read_b128 v[74:77], v74
	ds_read_b128 v[78:81], v78
	ds_read_b128 v[82:85], v221
	s_waitcnt lgkmcnt(0)
	v_mfma_f32_16x16x32_bf16 v[70:73], v[78:81], v[82:85], v[70:73]
	v_or_b32_e32 v78, v204, v183
	v_or_b32_e32 v180, 4, v232
	v_lshlrev_b32_e32 v181, 8, v180
	v_mfma_f32_16x16x32_bf16 v[66:69], v[74:77], v[82:85], v[66:69]
	v_lshl_or_b32 v74, v182, 10, v198
	ds_read_b128 v[74:77], v74
	ds_read_b128 v[78:81], v78
	ds_read_b128 v[82:85], v219
	s_waitcnt lgkmcnt(0)
	v_mfma_f32_16x16x32_bf16 v[66:69], v[74:77], v[82:85], v[66:69]
	v_lshl_or_b32 v74, v180, 10, v198
	ds_read_b128 v[74:77], v74
	v_or_b32_e32 v178, 5, v232
	v_mfma_f32_16x16x32_bf16 v[70:73], v[78:81], v[82:85], v[70:73]
	v_or_b32_e32 v78, v204, v181
	ds_read_b128 v[78:81], v78
	ds_read_b128 v[82:85], v218
	v_lshlrev_b32_e32 v179, 8, v178
	s_waitcnt lgkmcnt(0)
	v_mfma_f32_16x16x32_bf16 v[66:69], v[74:77], v[82:85], v[66:69]
	v_lshl_or_b32 v74, v178, 10, v198
	ds_read_b128 v[74:77], v74
	v_or_b32_e32 v176, 6, v232
	v_mfma_f32_16x16x32_bf16 v[70:73], v[78:81], v[82:85], v[70:73]
	v_or_b32_e32 v78, v204, v179
	ds_read_b128 v[78:81], v78
	ds_read_b128 v[82:85], v217
	v_lshlrev_b32_e32 v177, 8, v176
	s_waitcnt lgkmcnt(0)
	v_mfma_f32_16x16x32_bf16 v[66:69], v[74:77], v[82:85], v[66:69]
	v_lshl_or_b32 v74, v176, 10, v198
	ds_read_b128 v[74:77], v74
	v_or_b32_e32 v174, 7, v232
	v_mfma_f32_16x16x32_bf16 v[70:73], v[78:81], v[82:85], v[70:73]
	v_or_b32_e32 v78, v204, v177
	ds_read_b128 v[78:81], v78
	ds_read_b128 v[82:85], v216
	v_lshlrev_b32_e32 v175, 8, v174
	s_waitcnt lgkmcnt(0)
	v_mfma_f32_16x16x32_bf16 v[66:69], v[74:77], v[82:85], v[66:69]
	v_lshl_or_b32 v74, v174, 10, v198
	s_waitcnt vmcnt(16)
	v_cvt_pk_bf16_f32 v14, v14, v15
	v_cvt_pk_bf16_f32 v15, v16, v17
	v_mfma_f32_16x16x32_bf16 v[70:73], v[78:81], v[82:85], v[70:73]
	v_or_b32_e32 v78, v204, v175
	ds_read_b128 v[74:77], v74
	ds_read_b128 v[78:81], v78
	ds_read_b128 v[82:85], v213
	ds_write_b64 v209, v[14:15] offset:1536
	v_cvt_pk_bf16_f32 v14, v46, v47
	v_cvt_pk_bf16_f32 v15, v48, v49
	ds_write_b64 v208, v[14:15] offset:2048
	v_cvt_pk_bf16_f32 v14, v18, v19
	v_cvt_pk_bf16_f32 v15, v20, v21
	ds_write_b64 v207, v[14:15] offset:2560
	v_cvt_pk_bf16_f32 v14, v50, v51
	v_cvt_pk_bf16_f32 v15, v52, v53
	ds_write_b64 v206, v[14:15] offset:3072
	v_cvt_pk_bf16_f32 v14, v22, v23
	v_cvt_pk_bf16_f32 v15, v24, v25
	ds_write_b64 v205, v[14:15] offset:3584
	v_cvt_pk_bf16_f32 v14, v54, v55
	v_cvt_pk_bf16_f32 v15, v56, v57
	v_cvt_pk_bf16_f32 v6, v6, v7
	v_cvt_pk_bf16_f32 v2, v2, v3
	ds_write_b64 v231, v[14:15] offset:4096
	v_cvt_pk_bf16_f32 v14, v26, v27
	v_cvt_pk_bf16_f32 v15, v28, v29
	v_cvt_pk_bf16_f32 v7, v8, v9
	ds_write_b64 v226, v[6:7] offset:6656
	v_cvt_pk_bf16_f32 v6, v10, v11
	v_cvt_pk_bf16_f32 v3, v4, v5
	ds_write_b64 v224, v[2:3] offset:7680
	v_lshlrev_b32_e32 v2, 10, v235
	ds_write_b64 v230, v[14:15] offset:4608
	v_cvt_pk_bf16_f32 v14, v58, v59
	v_cvt_pk_bf16_f32 v15, v60, v61
	v_cvt_pk_bf16_f32 v7, v12, v13
	ds_write_b64 v225, v[6:7] offset:7168
	v_and_or_b32 v6, v2, s0, v203
	ds_write_b64 v229, v[14:15] offset:5120
	v_cvt_pk_bf16_f32 v14, v30, v31
	v_cvt_pk_bf16_f32 v15, v32, v33
	v_or_b32_e32 v7, 0x2000, v6
	ds_write_b64 v228, v[14:15] offset:5632
	v_cvt_pk_bf16_f32 v14, v34, v35
	v_cvt_pk_bf16_f32 v15, v36, v37
	buffer_load_dwordx4 v[2:5], v6, s[4:7], 0 offen nt
	buffer_load_dwordx4 v[10:13], v7, s[4:7], 0 offen nt
	v_or_b32_e32 v7, 0x4000, v6
	ds_write_b64 v227, v[14:15] offset:6144
	buffer_load_dwordx4 v[14:17], v7, s[4:7], 0 offen nt
	v_or_b32_e32 v7, 0x6000, v6
	v_cvt_pk_bf16_f32 v38, v38, v39
	v_cvt_pk_bf16_f32 v39, v40, v41
	buffer_load_dwordx4 v[22:25], v7, s[4:7], 0 offen nt
	v_or_b32_e32 v7, 0x8000, v6
	ds_write_b64 v211, v[38:39] offset:512
	v_cvt_pk_bf16_f32 v38, v42, v43
	v_cvt_pk_bf16_f32 v39, v44, v45
	buffer_load_dwordx4 v[30:33], v7, s[4:7], 0 offen nt
	v_or_b32_e32 v7, 0xa000, v6
	ds_write_b64 v210, v[38:39] offset:1024
	buffer_load_dwordx4 v[38:41], v7, s[4:7], 0 offen nt
	v_or_b32_e32 v7, 0xc000, v6
	buffer_load_dwordx4 v[46:49], v7, s[4:7], 0 offen nt
	v_or_b32_e32 v7, 0xe000, v6
	v_cvt_pk_bf16_f32 v62, v62, v63
	v_cvt_pk_bf16_f32 v63, v64, v65
	buffer_load_dwordx4 v[54:57], v7, s[4:7], 0 offen nt
	v_or_b32_e32 v7, 0x10000, v6
	ds_write_b64 v212, v[62:63]
	buffer_load_dwordx4 v[62:65], v7, s[4:7], 0 offen nt
	v_or_b32_e32 v7, 0x12000, v6
	s_waitcnt lgkmcnt(14)
	v_mfma_f32_16x16x32_bf16 v[66:69], v[74:77], v[82:85], v[66:69]
	v_mfma_f32_16x16x32_bf16 v[74:77], v[78:81], v[82:85], v[70:73]
	s_nop 2
	buffer_load_dwordx4 v[70:73], v7, s[4:7], 0 offen nt
	v_or_b32_e32 v7, 0x14000, v6
	buffer_load_dwordx4 v[78:81], v7, s[4:7], 0 offen nt
	v_or_b32_e32 v7, 0x16000, v6
	buffer_load_dwordx4 v[86:89], v7, s[4:7], 0 offen nt
	v_or_b32_e32 v7, 0x18000, v6
	buffer_load_dwordx4 v[94:97], v7, s[4:7], 0 offen nt
	v_or_b32_e32 v7, 0x1a000, v6
	buffer_load_dwordx4 v[146:149], v7, s[4:7], 0 offen nt
	v_or_b32_e32 v7, 0x1c000, v6
	v_or_b32_e32 v6, 0x1e000, v6
	buffer_load_dwordx4 v[150:153], v7, s[4:7], 0 offen nt
	buffer_load_dwordx4 v[154:157], v6, s[4:7], 0 offen nt
	v_add_u32_e32 v6, 8, v232
	v_and_b32_e32 v50, 56, v6
	v_lshl_or_b32 v6, v50, 10, v198
	ds_read_b128 v[6:9], v6
	v_lshl_or_b32 v18, v50, 8, v204
	ds_read_b128 v[18:21], v18
	ds_read_b128 v[26:29], v223
	v_or_b32_e32 v34, 1, v50
	s_movk_i32 s24, 0x1000
	s_waitcnt lgkmcnt(0)
	v_mfma_f32_16x16x32_bf16 v[18:21], v[18:21], v[26:29], v[74:77]
	v_add_u32_e32 v234, 5, v200
	v_mfma_f32_16x16x32_bf16 v[6:9], v[6:9], v[26:29], v[66:69]
	v_lshl_or_b32 v26, v34, 10, v198
	ds_read_b128 v[26:29], v26
	v_lshl_or_b32 v34, v34, 8, v204
	ds_read_b128 v[34:37], v34
	ds_read_b128 v[42:45], v222
	s_waitcnt lgkmcnt(0)
	v_mfma_f32_16x16x32_bf16 v[18:21], v[34:37], v[42:45], v[18:21]
	v_or_b32_e32 v34, 2, v50
	v_mfma_f32_16x16x32_bf16 v[6:9], v[26:29], v[42:45], v[6:9]
	v_lshl_or_b32 v26, v34, 10, v198
	ds_read_b128 v[26:29], v26
	v_lshl_or_b32 v34, v34, 8, v204
	ds_read_b128 v[34:37], v34
	ds_read_b128 v[42:45], v221
	s_waitcnt lgkmcnt(0)
	v_mfma_f32_16x16x32_bf16 v[18:21], v[34:37], v[42:45], v[18:21]
	v_or_b32_e32 v34, 3, v50
	v_mfma_f32_16x16x32_bf16 v[6:9], v[26:29], v[42:45], v[6:9]
	v_lshl_or_b32 v26, v34, 10, v198
	ds_read_b128 v[26:29], v26
	v_lshl_or_b32 v34, v34, 8, v204
	ds_read_b128 v[34:37], v34
	ds_read_b128 v[42:45], v219
	s_waitcnt lgkmcnt(0)
	v_mfma_f32_16x16x32_bf16 v[18:21], v[34:37], v[42:45], v[18:21]
	v_or_b32_e32 v34, 4, v50
	v_mfma_f32_16x16x32_bf16 v[6:9], v[26:29], v[42:45], v[6:9]
	v_lshl_or_b32 v26, v34, 10, v198
	ds_read_b128 v[26:29], v26
	v_lshl_or_b32 v34, v34, 8, v204
	ds_read_b128 v[34:37], v34
	ds_read_b128 v[42:45], v218
	s_waitcnt lgkmcnt(0)
	v_mfma_f32_16x16x32_bf16 v[18:21], v[34:37], v[42:45], v[18:21]
	v_or_b32_e32 v34, 5, v50
	v_mfma_f32_16x16x32_bf16 v[6:9], v[26:29], v[42:45], v[6:9]
	v_lshl_or_b32 v26, v34, 10, v198
	ds_read_b128 v[26:29], v26
	v_lshl_or_b32 v34, v34, 8, v204
	ds_read_b128 v[34:37], v34
	ds_read_b128 v[42:45], v217
	s_waitcnt lgkmcnt(0)
	v_mfma_f32_16x16x32_bf16 v[18:21], v[34:37], v[42:45], v[18:21]
	v_or_b32_e32 v34, 6, v50
	v_mfma_f32_16x16x32_bf16 v[6:9], v[26:29], v[42:45], v[6:9]
	v_lshl_or_b32 v26, v34, 10, v198
	ds_read_b128 v[26:29], v26
	v_lshl_or_b32 v34, v34, 8, v204
	ds_read_b128 v[34:37], v34
	ds_read_b128 v[42:45], v216
	s_waitcnt lgkmcnt(0)
	v_mfma_f32_16x16x32_bf16 v[18:21], v[34:37], v[42:45], v[18:21]
	v_or_b32_e32 v34, 7, v50
	v_mfma_f32_16x16x32_bf16 v[6:9], v[26:29], v[42:45], v[6:9]
	v_lshl_or_b32 v26, v34, 10, v198
	ds_read_b128 v[26:29], v26
	v_lshl_or_b32 v34, v34, 8, v204
	ds_read_b128 v[34:37], v34
	ds_read_b128 v[42:45], v213
	s_waitcnt lgkmcnt(0)
	v_mfma_f32_16x16x32_bf16 v[162:165], v[26:29], v[42:45], v[6:9]
	s_waitcnt vmcnt(31)
	s_nop 1
	v_cvt_pk_bf16_f32 v6, v102, v103
	v_cvt_pk_bf16_f32 v7, v104, v105
	ds_write_b64 v212, v[6:7]
	s_waitcnt vmcnt(30)
	v_cvt_pk_bf16_f32 v6, v98, v99
	v_cvt_pk_bf16_f32 v7, v100, v101
	ds_write_b64 v211, v[6:7] offset:512
	s_waitcnt vmcnt(29)
	v_cvt_pk_bf16_f32 v6, v110, v111
	v_cvt_pk_bf16_f32 v7, v112, v113
	ds_write_b64 v210, v[6:7] offset:1024
	s_waitcnt vmcnt(28)
	v_cvt_pk_bf16_f32 v6, v106, v107
	v_cvt_pk_bf16_f32 v7, v108, v109
	ds_write_b64 v209, v[6:7] offset:1536
	s_waitcnt vmcnt(27)
	v_cvt_pk_bf16_f32 v6, v118, v119
	v_cvt_pk_bf16_f32 v7, v120, v121
	ds_write_b64 v208, v[6:7] offset:2048
	s_waitcnt vmcnt(26)
	v_cvt_pk_bf16_f32 v6, v114, v115
	v_cvt_pk_bf16_f32 v7, v116, v117
	ds_write_b64 v207, v[6:7] offset:2560
	s_waitcnt vmcnt(25)
	v_cvt_pk_bf16_f32 v6, v126, v127
	v_cvt_pk_bf16_f32 v7, v128, v129
	ds_write_b64 v206, v[6:7] offset:3072
	s_waitcnt vmcnt(24)
	v_cvt_pk_bf16_f32 v6, v122, v123
	v_cvt_pk_bf16_f32 v7, v124, v125
	ds_write_b64 v205, v[6:7] offset:3584
	s_waitcnt vmcnt(23)
	v_cvt_pk_bf16_f32 v6, v134, v135
	v_cvt_pk_bf16_f32 v7, v136, v137
	ds_write_b64 v231, v[6:7] offset:4096
	s_waitcnt vmcnt(22)
	v_cvt_pk_bf16_f32 v6, v130, v131
	v_cvt_pk_bf16_f32 v7, v132, v133
	ds_write_b64 v230, v[6:7] offset:4608
	s_waitcnt vmcnt(21)
	v_cvt_pk_bf16_f32 v6, v142, v143
	v_cvt_pk_bf16_f32 v7, v144, v145
	ds_write_b64 v229, v[6:7] offset:5120
	s_waitcnt vmcnt(20)
	v_cvt_pk_bf16_f32 v6, v138, v139
	v_cvt_pk_bf16_f32 v7, v140, v141
	ds_write_b64 v228, v[6:7] offset:5632
	s_waitcnt vmcnt(19)
	v_cvt_pk_bf16_f32 v6, v170, v171
	v_cvt_pk_bf16_f32 v7, v172, v173
	ds_write_b64 v227, v[6:7] offset:6144
	s_waitcnt vmcnt(18)
	v_cvt_pk_bf16_f32 v6, v158, v159
	v_mov_b32_e32 v106, 0x1000
	v_cvt_pk_bf16_f32 v7, v160, v161
	ds_write_b64 v226, v[6:7] offset:6656
	s_waitcnt vmcnt(17)
	v_cvt_pk_bf16_f32 v6, v190, v191
	v_bitop3_b32 v107, v233, s19, v106 bitop3:0xde
	v_mfma_f32_16x16x32_bf16 v[166:169], v[34:37], v[42:45], v[18:21]
	v_cvt_pk_bf16_f32 v7, v192, v193
	ds_write_b64 v225, v[6:7] offset:7168
	s_waitcnt vmcnt(16)
	v_cvt_pk_bf16_f32 v6, v186, v187
	v_bitop3_b32 v26, v233, s17, v106 bitop3:0xde
	v_bitop3_b32 v34, v233, s11, v106 bitop3:0xde
	v_bitop3_b32 v18, v233, s16, v106 bitop3:0xde
	v_bitop3_b32 v42, v233, s13, v106 bitop3:0xde
	v_bitop3_b32 v50, v233, s10, v106 bitop3:0xde
	v_bitop3_b32 v58, v233, s12, v106 bitop3:0xde
	v_bitop3_b32 v66, v233, s1, v106 bitop3:0xde
	v_bitop3_b32 v74, v233, s18, v106 bitop3:0xde
	v_bitop3_b32 v82, v233, s23, v106 bitop3:0xde
	v_bitop3_b32 v90, v233, s22, v106 bitop3:0xde
	v_bitop3_b32 v98, v233, s21, v106 bitop3:0xde
	v_bitop3_b32 v102, v233, s20, v106 bitop3:0xde
	buffer_load_dwordx4 v[110:113], v107, s[4:7], 0 offen nt
	v_bitop3_b32 v107, v233, s15, v106 bitop3:0xde
	v_bitop3_b32 v106, v233, s14, v106 bitop3:0xde
	v_cvt_pk_bf16_f32 v7, v188, v189
	ds_write_b64 v224, v[6:7] offset:7680
	v_bitop3_b32 v6, v203, s24, v196 bitop3:0x36
	buffer_load_dwordx4 v[42:45], v42, s[4:7], 0 offen nt
	s_nop 0
	buffer_load_dwordx4 v[50:53], v50, s[4:7], 0 offen nt
	s_nop 0
	buffer_load_dwordx4 v[58:61], v58, s[4:7], 0 offen nt
	s_nop 0
	buffer_load_dwordx4 v[66:69], v66, s[4:7], 0 offen nt
	s_nop 0
	buffer_load_dwordx4 v[74:77], v74, s[4:7], 0 offen nt
	s_nop 0
	buffer_load_dwordx4 v[82:85], v82, s[4:7], 0 offen nt
	s_nop 0
	buffer_load_dwordx4 v[90:93], v90, s[4:7], 0 offen nt
	s_nop 0
	buffer_load_dwordx4 v[98:101], v98, s[4:7], 0 offen nt
	s_nop 0
	buffer_load_dwordx4 v[102:105], v102, s[4:7], 0 offen nt
	s_nop 0
	buffer_load_dwordx4 v[126:129], v106, s[4:7], 0 offen nt
	buffer_load_dwordx4 v[118:121], v107, s[4:7], 0 offen nt
	s_nop 0
	buffer_load_dwordx4 v[6:9], v6, s[4:7], 0 offen nt
	s_nop 0
	buffer_load_dwordx4 v[18:21], v18, s[4:7], 0 offen nt
	s_nop 0
	buffer_load_dwordx4 v[26:29], v26, s[4:7], 0 offen nt
	s_nop 0
	buffer_load_dwordx4 v[34:37], v34, s[4:7], 0 offen nt
	v_add_u32_e32 v106, 16, v232
	v_and_b32_e32 v138, 56, v106
	v_lshl_or_b32 v106, v138, 10, v198
	ds_read_b128 v[106:109], v106
	v_lshl_or_b32 v114, v138, 8, v204
	ds_read_b128 v[114:117], v114
	ds_read_b128 v[122:125], v223
	v_or_b32_e32 v130, 1, v138
	s_waitcnt vmcnt(31)
	v_cvt_pk_bf16_f32 v2, v2, v3
	s_waitcnt lgkmcnt(0)
	v_mfma_f32_16x16x32_bf16 v[114:117], v[114:117], v[122:125], v[166:169]
	v_cvt_pk_bf16_f32 v3, v4, v5
	v_mfma_f32_16x16x32_bf16 v[106:109], v[106:109], v[122:125], v[162:165]
	v_lshl_or_b32 v122, v130, 10, v198
	ds_read_b128 v[122:125], v122
	v_lshl_or_b32 v130, v130, 8, v204
	ds_read_b128 v[130:133], v130
	ds_read_b128 v[134:137], v222
	s_waitcnt lgkmcnt(0)
	v_mfma_f32_16x16x32_bf16 v[114:117], v[130:133], v[134:137], v[114:117]
	v_or_b32_e32 v130, 2, v138
	v_mfma_f32_16x16x32_bf16 v[106:109], v[122:125], v[134:137], v[106:109]
	v_lshl_or_b32 v122, v130, 10, v198
	ds_read_b128 v[122:125], v122
	v_lshl_or_b32 v130, v130, 8, v204
	ds_read_b128 v[130:133], v130
	ds_read_b128 v[134:137], v221
	s_waitcnt lgkmcnt(0)
	v_mfma_f32_16x16x32_bf16 v[114:117], v[130:133], v[134:137], v[114:117]
	v_or_b32_e32 v130, 3, v138
	v_mfma_f32_16x16x32_bf16 v[106:109], v[122:125], v[134:137], v[106:109]
	v_lshl_or_b32 v122, v130, 10, v198
	ds_read_b128 v[122:125], v122
	v_lshl_or_b32 v130, v130, 8, v204
	ds_read_b128 v[130:133], v130
	ds_read_b128 v[134:137], v219
	s_waitcnt lgkmcnt(0)
	v_mfma_f32_16x16x32_bf16 v[114:117], v[130:133], v[134:137], v[114:117]
	v_or_b32_e32 v130, 4, v138
	v_mfma_f32_16x16x32_bf16 v[106:109], v[122:125], v[134:137], v[106:109]
	v_lshl_or_b32 v122, v130, 10, v198
	ds_read_b128 v[122:125], v122
	v_lshl_or_b32 v130, v130, 8, v204
	ds_read_b128 v[130:133], v130
	ds_read_b128 v[134:137], v218
	s_waitcnt lgkmcnt(0)
	v_mfma_f32_16x16x32_bf16 v[114:117], v[130:133], v[134:137], v[114:117]
	v_or_b32_e32 v130, 5, v138
	v_mfma_f32_16x16x32_bf16 v[106:109], v[122:125], v[134:137], v[106:109]
	v_lshl_or_b32 v122, v130, 10, v198
	ds_read_b128 v[122:125], v122
	v_lshl_or_b32 v130, v130, 8, v204
	ds_read_b128 v[130:133], v130
	ds_read_b128 v[134:137], v217
	s_waitcnt lgkmcnt(0)
	v_mfma_f32_16x16x32_bf16 v[114:117], v[130:133], v[134:137], v[114:117]
	v_or_b32_e32 v130, 6, v138
	v_mfma_f32_16x16x32_bf16 v[106:109], v[122:125], v[134:137], v[106:109]
	v_lshl_or_b32 v122, v130, 10, v198
	ds_read_b128 v[122:125], v122
	v_lshl_or_b32 v130, v130, 8, v204
	ds_read_b128 v[130:133], v130
	ds_read_b128 v[134:137], v216
	s_waitcnt lgkmcnt(0)
	v_mfma_f32_16x16x32_bf16 v[114:117], v[130:133], v[134:137], v[114:117]
	v_or_b32_e32 v130, 7, v138
	v_mfma_f32_16x16x32_bf16 v[106:109], v[122:125], v[134:137], v[106:109]
	v_lshl_or_b32 v122, v130, 10, v198
	v_lshl_or_b32 v130, v130, 8, v204
	ds_read_b128 v[122:125], v122
	ds_read_b128 v[134:137], v130
	ds_read_b128 v[138:141], v213
	ds_write_b64 v212, v[2:3]
	s_waitcnt vmcnt(30)
	v_cvt_pk_bf16_f32 v2, v10, v11
	v_cvt_pk_bf16_f32 v3, v12, v13
	ds_write_b64 v211, v[2:3] offset:512
	s_waitcnt vmcnt(29)
	v_cvt_pk_bf16_f32 v2, v14, v15
	v_cvt_pk_bf16_f32 v3, v16, v17
	ds_write_b64 v210, v[2:3] offset:1024
	s_waitcnt vmcnt(28)
	v_cvt_pk_bf16_f32 v2, v22, v23
	v_cvt_pk_bf16_f32 v3, v24, v25
	ds_write_b64 v209, v[2:3] offset:1536
	s_waitcnt vmcnt(27)
	v_cvt_pk_bf16_f32 v2, v30, v31
	v_cvt_pk_bf16_f32 v3, v32, v33
	ds_write_b64 v208, v[2:3] offset:2048
	s_waitcnt vmcnt(26)
	v_cvt_pk_bf16_f32 v2, v38, v39
	v_cvt_pk_bf16_f32 v3, v40, v41
	ds_write_b64 v207, v[2:3] offset:2560
	s_waitcnt vmcnt(25)
	v_cvt_pk_bf16_f32 v2, v46, v47
	v_cvt_pk_bf16_f32 v3, v48, v49
	ds_write_b64 v206, v[2:3] offset:3072
	s_waitcnt vmcnt(24)
	v_cvt_pk_bf16_f32 v2, v54, v55
	v_cvt_pk_bf16_f32 v3, v56, v57
	ds_write_b64 v205, v[2:3] offset:3584
	s_waitcnt vmcnt(23)
	v_cvt_pk_bf16_f32 v2, v62, v63
	v_cvt_pk_bf16_f32 v3, v64, v65
	ds_write_b64 v231, v[2:3] offset:4096
	s_waitcnt vmcnt(22)
	v_cvt_pk_bf16_f32 v2, v70, v71
	v_cvt_pk_bf16_f32 v3, v72, v73
	ds_write_b64 v230, v[2:3] offset:4608
	s_waitcnt vmcnt(21)
	v_cvt_pk_bf16_f32 v2, v78, v79
	v_cvt_pk_bf16_f32 v3, v80, v81
	ds_write_b64 v229, v[2:3] offset:5120
	s_waitcnt vmcnt(20)
	v_cvt_pk_bf16_f32 v2, v86, v87
	v_cvt_pk_bf16_f32 v3, v88, v89
	ds_write_b64 v228, v[2:3] offset:5632
	s_waitcnt vmcnt(19)
	v_cvt_pk_bf16_f32 v2, v94, v95
	v_cvt_pk_bf16_f32 v3, v96, v97
	ds_write_b64 v227, v[2:3] offset:6144
	s_waitcnt vmcnt(18)
	v_cvt_pk_bf16_f32 v2, v146, v147
	v_cvt_pk_bf16_f32 v3, v148, v149
	ds_write_b64 v226, v[2:3] offset:6656
	s_waitcnt vmcnt(17)
	v_cvt_pk_bf16_f32 v2, v150, v151
	v_cvt_pk_bf16_f32 v3, v152, v153
	ds_write_b64 v225, v[2:3] offset:7168
	s_waitcnt vmcnt(16)
	v_cvt_pk_bf16_f32 v2, v154, v155
	v_cvt_pk_bf16_f32 v3, v156, v157
	ds_write_b64 v224, v[2:3] offset:7680
	v_lshlrev_b32_e32 v2, 10, v234
	s_waitcnt lgkmcnt(14)
	v_mfma_f32_16x16x32_bf16 v[130:133], v[122:125], v[138:141], v[106:109]
	v_and_or_b32 v122, v2, s0, v203
	buffer_load_dwordx4 v[2:5], v122, s[4:7], 0 offen nt
	v_or_b32_e32 v10, 0x2000, v122
	v_mfma_f32_16x16x32_bf16 v[134:137], v[134:137], v[138:141], v[114:117]
	v_or_b32_e32 v14, 0x4000, v122
	v_or_b32_e32 v22, 0x6000, v122
	v_or_b32_e32 v30, 0x8000, v122
	v_or_b32_e32 v38, 0xa000, v122
	v_or_b32_e32 v46, 0xc000, v122
	v_or_b32_e32 v54, 0xe000, v122
	v_or_b32_e32 v62, 0x10000, v122
	v_or_b32_e32 v70, 0x12000, v122
	v_or_b32_e32 v78, 0x14000, v122
	v_or_b32_e32 v86, 0x16000, v122
	v_or_b32_e32 v94, 0x18000, v122
	v_or_b32_e32 v106, 0x1a000, v122
	v_or_b32_e32 v114, 0x1c000, v122
	v_or_b32_e32 v122, 0x1e000, v122
	buffer_load_dwordx4 v[54:57], v54, s[4:7], 0 offen nt
	s_nop 0
	buffer_load_dwordx4 v[62:65], v62, s[4:7], 0 offen nt
	s_nop 0
	buffer_load_dwordx4 v[70:73], v70, s[4:7], 0 offen nt
	s_nop 0
	buffer_load_dwordx4 v[78:81], v78, s[4:7], 0 offen nt
	s_nop 0
	buffer_load_dwordx4 v[86:89], v86, s[4:7], 0 offen nt
	s_nop 0
	buffer_load_dwordx4 v[94:97], v94, s[4:7], 0 offen nt
	s_nop 0
	buffer_load_dwordx4 v[106:109], v106, s[4:7], 0 offen nt
	s_nop 0
	buffer_load_dwordx4 v[114:117], v114, s[4:7], 0 offen nt
	s_nop 0
	buffer_load_dwordx4 v[122:125], v122, s[4:7], 0 offen nt
	s_nop 0
	buffer_load_dwordx4 v[10:13], v10, s[4:7], 0 offen nt
	s_nop 0
	buffer_load_dwordx4 v[14:17], v14, s[4:7], 0 offen nt
	s_nop 0
	buffer_load_dwordx4 v[22:25], v22, s[4:7], 0 offen nt
	s_nop 0
	buffer_load_dwordx4 v[30:33], v30, s[4:7], 0 offen nt
	s_nop 0
	buffer_load_dwordx4 v[38:41], v38, s[4:7], 0 offen nt
	s_nop 0
	buffer_load_dwordx4 v[46:49], v46, s[4:7], 0 offen nt
	v_lshlrev_b32_e32 v138, 3, v235
	v_and_b32_e32 v150, 56, v138
	v_lshl_or_b32 v138, v150, 10, v198
	ds_read_b128 v[138:141], v138
	v_lshl_or_b32 v142, v150, 8, v204
	ds_read_b128 v[142:145], v142
	ds_read_b128 v[146:149], v223
	s_waitcnt vmcnt(19)
	v_cvt_pk_bf16_f32 v6, v6, v7
	v_cvt_pk_bf16_f32 v7, v8, v9
	s_waitcnt lgkmcnt(0)
	v_mfma_f32_16x16x32_bf16 v[134:137], v[142:145], v[146:149], v[134:137]
	v_or_b32_e32 v142, 1, v150
	v_mfma_f32_16x16x32_bf16 v[130:133], v[138:141], v[146:149], v[130:133]
	v_lshl_or_b32 v138, v142, 10, v198
	ds_read_b128 v[138:141], v138
	v_lshl_or_b32 v142, v142, 8, v204
	ds_read_b128 v[142:145], v142
	ds_read_b128 v[146:149], v222
	s_waitcnt lgkmcnt(0)
	v_mfma_f32_16x16x32_bf16 v[134:137], v[142:145], v[146:149], v[134:137]
	v_or_b32_e32 v142, 2, v150
	v_mfma_f32_16x16x32_bf16 v[130:133], v[138:141], v[146:149], v[130:133]
	v_lshl_or_b32 v138, v142, 10, v198
	ds_read_b128 v[138:141], v138
	v_lshl_or_b32 v142, v142, 8, v204
	ds_read_b128 v[142:145], v142
	ds_read_b128 v[146:149], v221
	s_waitcnt lgkmcnt(0)
	v_mfma_f32_16x16x32_bf16 v[134:137], v[142:145], v[146:149], v[134:137]
	v_or_b32_e32 v142, 3, v150
	v_mfma_f32_16x16x32_bf16 v[130:133], v[138:141], v[146:149], v[130:133]
	v_lshl_or_b32 v138, v142, 10, v198
	ds_read_b128 v[138:141], v138
	v_lshl_or_b32 v142, v142, 8, v204
	ds_read_b128 v[142:145], v142
	ds_read_b128 v[146:149], v219
	s_waitcnt lgkmcnt(0)
	v_mfma_f32_16x16x32_bf16 v[134:137], v[142:145], v[146:149], v[134:137]
	v_or_b32_e32 v142, 4, v150
	v_mfma_f32_16x16x32_bf16 v[130:133], v[138:141], v[146:149], v[130:133]
	v_lshl_or_b32 v138, v142, 10, v198
	ds_read_b128 v[138:141], v138
	v_lshl_or_b32 v142, v142, 8, v204
	ds_read_b128 v[142:145], v142
	ds_read_b128 v[146:149], v218
	s_waitcnt lgkmcnt(0)
	v_mfma_f32_16x16x32_bf16 v[134:137], v[142:145], v[146:149], v[134:137]
	v_or_b32_e32 v142, 5, v150
	v_mfma_f32_16x16x32_bf16 v[130:133], v[138:141], v[146:149], v[130:133]
	v_lshl_or_b32 v138, v142, 10, v198
	ds_read_b128 v[138:141], v138
	v_lshl_or_b32 v142, v142, 8, v204
	ds_read_b128 v[142:145], v142
	ds_read_b128 v[146:149], v217
	s_waitcnt lgkmcnt(0)
	v_mfma_f32_16x16x32_bf16 v[134:137], v[142:145], v[146:149], v[134:137]
	v_or_b32_e32 v142, 6, v150
	v_mfma_f32_16x16x32_bf16 v[130:133], v[138:141], v[146:149], v[130:133]
	v_lshl_or_b32 v138, v142, 10, v198
	ds_read_b128 v[138:141], v138
	v_lshl_or_b32 v142, v142, 8, v204
	ds_read_b128 v[142:145], v142
	ds_read_b128 v[146:149], v216
	s_waitcnt lgkmcnt(0)
	v_mfma_f32_16x16x32_bf16 v[134:137], v[142:145], v[146:149], v[134:137]
	v_or_b32_e32 v142, 7, v150
	v_mfma_f32_16x16x32_bf16 v[130:133], v[138:141], v[146:149], v[130:133]
	v_lshl_or_b32 v138, v142, 10, v198
	v_lshl_or_b32 v142, v142, 8, v204
	ds_read_b128 v[138:141], v138
	ds_read_b128 v[142:145], v142
	ds_read_b128 v[146:149], v213
	ds_write_b64 v212, v[6:7]
	s_waitcnt vmcnt(18)
	v_cvt_pk_bf16_f32 v6, v18, v19
	v_cvt_pk_bf16_f32 v7, v20, v21
	ds_write_b64 v211, v[6:7] offset:512
	s_waitcnt vmcnt(17)
	v_cvt_pk_bf16_f32 v6, v26, v27
	v_cvt_pk_bf16_f32 v7, v28, v29
	ds_write_b64 v210, v[6:7] offset:1024
	s_waitcnt vmcnt(16)
	v_cvt_pk_bf16_f32 v6, v34, v35
	v_cvt_pk_bf16_f32 v7, v36, v37
	ds_write_b64 v209, v[6:7] offset:1536
	v_cvt_pk_bf16_f32 v6, v42, v43
	v_cvt_pk_bf16_f32 v7, v44, v45
	ds_write_b64 v208, v[6:7] offset:2048
	v_cvt_pk_bf16_f32 v6, v50, v51
	v_cvt_pk_bf16_f32 v7, v52, v53
	ds_write_b64 v207, v[6:7] offset:2560
	v_cvt_pk_bf16_f32 v6, v58, v59
	v_cvt_pk_bf16_f32 v7, v60, v61
	ds_write_b64 v206, v[6:7] offset:3072
	v_cvt_pk_bf16_f32 v6, v66, v67
	v_cvt_pk_bf16_f32 v7, v68, v69
	ds_write_b64 v205, v[6:7] offset:3584
	v_cvt_pk_bf16_f32 v6, v74, v75
	v_cvt_pk_bf16_f32 v7, v76, v77
	ds_write_b64 v231, v[6:7] offset:4096
	v_cvt_pk_bf16_f32 v6, v82, v83
	v_cvt_pk_bf16_f32 v7, v84, v85
	ds_write_b64 v230, v[6:7] offset:4608
	v_cvt_pk_bf16_f32 v6, v90, v91
	v_cvt_pk_bf16_f32 v7, v92, v93
	ds_write_b64 v229, v[6:7] offset:5120
	v_cvt_pk_bf16_f32 v6, v98, v99
	v_cvt_pk_bf16_f32 v7, v100, v101
	ds_write_b64 v228, v[6:7] offset:5632
	v_cvt_pk_bf16_f32 v6, v102, v103
	v_cvt_pk_bf16_f32 v7, v104, v105
	ds_write_b64 v227, v[6:7] offset:6144
	v_cvt_pk_bf16_f32 v6, v110, v111
	v_cvt_pk_bf16_f32 v7, v112, v113
	ds_write_b64 v226, v[6:7] offset:6656
	v_cvt_pk_bf16_f32 v6, v118, v119
	v_cvt_pk_bf16_f32 v7, v120, v121
	ds_write_b64 v225, v[6:7] offset:7168
	v_cvt_pk_bf16_f32 v6, v126, v127
	v_cvt_pk_bf16_f32 v7, v128, v129
	ds_write_b64 v224, v[6:7] offset:7680
	v_add_u32_e32 v6, 0x1800, v196
	v_and_or_b32 v126, v6, s0, v203
	buffer_load_dwordx4 v[6:9], v126, s[4:7], 0 offen nt
	v_or_b32_e32 v18, 0x2000, v126
	v_or_b32_e32 v26, 0x4000, v126
	v_or_b32_e32 v34, 0x6000, v126
	v_or_b32_e32 v42, 0x8000, v126
	v_or_b32_e32 v50, 0xa000, v126
	v_or_b32_e32 v58, 0xc000, v126
	v_or_b32_e32 v66, 0xe000, v126
	v_or_b32_e32 v74, 0x10000, v126
	v_or_b32_e32 v82, 0x12000, v126
	v_or_b32_e32 v90, 0x14000, v126
	v_or_b32_e32 v98, 0x16000, v126
	v_or_b32_e32 v102, 0x18000, v126
	v_or_b32_e32 v110, 0x1a000, v126
	v_or_b32_e32 v118, 0x1c000, v126
	v_or_b32_e32 v126, 0x1e000, v126
	buffer_load_dwordx4 v[50:53], v50, s[4:7], 0 offen nt
	s_waitcnt lgkmcnt(14)
	v_mfma_f32_16x16x32_bf16 v[130:133], v[138:141], v[146:149], v[130:133]
	buffer_load_dwordx4 v[58:61], v58, s[4:7], 0 offen nt
	s_nop 0
	buffer_load_dwordx4 v[66:69], v66, s[4:7], 0 offen nt
	v_mfma_f32_16x16x32_bf16 v[134:137], v[142:145], v[146:149], v[134:137]
	buffer_load_dwordx4 v[74:77], v74, s[4:7], 0 offen nt
	v_add_u32_e32 v142, 7, v200
	buffer_load_dwordx4 v[82:85], v82, s[4:7], 0 offen nt
	s_nop 0
	buffer_load_dwordx4 v[90:93], v90, s[4:7], 0 offen nt
	s_nop 0
	buffer_load_dwordx4 v[98:101], v98, s[4:7], 0 offen nt
	s_nop 0
	buffer_load_dwordx4 v[102:105], v102, s[4:7], 0 offen nt
	s_nop 0
	buffer_load_dwordx4 v[110:113], v110, s[4:7], 0 offen nt
	s_nop 0
	buffer_load_dwordx4 v[118:121], v118, s[4:7], 0 offen nt
	s_nop 0
	buffer_load_dwordx4 v[126:129], v126, s[4:7], 0 offen nt
	s_nop 0
	buffer_load_dwordx4 v[18:21], v18, s[4:7], 0 offen nt
	s_nop 0
	buffer_load_dwordx4 v[26:29], v26, s[4:7], 0 offen nt
	s_nop 0
	buffer_load_dwordx4 v[34:37], v34, s[4:7], 0 offen nt
	s_nop 0
	buffer_load_dwordx4 v[42:45], v42, s[4:7], 0 offen nt
	v_xor_b32_e32 v143, 32, v232
	v_lshl_or_b32 v138, v143, 10, v198
	ds_read_b128 v[138:141], v138
	v_lshl_or_b32 v143, v143, 8, v204
	ds_read_b128 v[144:147], v143
	ds_read_b128 v[148:151], v223
	v_bitop3_b32 v143, v232, 1, 32 bitop3:0xde
	s_waitcnt vmcnt(31)
	v_cvt_pk_bf16_f32 v2, v2, v3
	s_waitcnt lgkmcnt(0)
	v_mfma_f32_16x16x32_bf16 v[134:137], v[144:147], v[148:151], v[134:137]
	v_cvt_pk_bf16_f32 v3, v4, v5
	v_mfma_f32_16x16x32_bf16 v[130:133], v[138:141], v[148:151], v[130:133]
	v_lshl_or_b32 v138, v143, 10, v198
	ds_read_b128 v[138:141], v138
	v_lshl_or_b32 v143, v143, 8, v204
	ds_read_b128 v[144:147], v143
	ds_read_b128 v[148:151], v222
	v_bitop3_b32 v143, v232, 2, 32 bitop3:0xde
	s_waitcnt lgkmcnt(0)
	v_mfma_f32_16x16x32_bf16 v[134:137], v[144:147], v[148:151], v[134:137]
	v_mfma_f32_16x16x32_bf16 v[130:133], v[138:141], v[148:151], v[130:133]
	v_lshl_or_b32 v138, v143, 10, v198
	ds_read_b128 v[138:141], v138
	v_lshl_or_b32 v143, v143, 8, v204
	ds_read_b128 v[144:147], v143
	ds_read_b128 v[148:151], v221
	v_bitop3_b32 v143, v232, 3, 32 bitop3:0xde
	s_waitcnt lgkmcnt(0)
	v_mfma_f32_16x16x32_bf16 v[130:133], v[138:141], v[148:151], v[130:133]
	v_lshl_or_b32 v138, v143, 10, v198
	ds_read_b128 v[138:141], v138
	v_lshl_or_b32 v143, v143, 8, v204
	v_mfma_f32_16x16x32_bf16 v[134:137], v[144:147], v[148:151], v[134:137]
	ds_read_b128 v[144:147], v143
	ds_read_b128 v[148:151], v219
	v_bitop3_b32 v143, v232, 4, 32 bitop3:0xde
	s_waitcnt lgkmcnt(0)
	v_mfma_f32_16x16x32_bf16 v[130:133], v[138:141], v[148:151], v[130:133]
	v_lshl_or_b32 v138, v143, 10, v198
	ds_read_b128 v[138:141], v138
	v_lshl_or_b32 v143, v143, 8, v204
	v_mfma_f32_16x16x32_bf16 v[134:137], v[144:147], v[148:151], v[134:137]
	ds_read_b128 v[144:147], v143
	ds_read_b128 v[148:151], v218
	v_bitop3_b32 v143, v232, 5, 32 bitop3:0xde
	s_waitcnt lgkmcnt(0)
	v_mfma_f32_16x16x32_bf16 v[130:133], v[138:141], v[148:151], v[130:133]
	v_lshl_or_b32 v138, v143, 10, v198
	ds_read_b128 v[138:141], v138
	v_lshl_or_b32 v143, v143, 8, v204
	v_mfma_f32_16x16x32_bf16 v[134:137], v[144:147], v[148:151], v[134:137]
	ds_read_b128 v[144:147], v143
	ds_read_b128 v[148:151], v217
	v_bitop3_b32 v143, v232, 6, 32 bitop3:0xde
	s_waitcnt lgkmcnt(0)
	v_mfma_f32_16x16x32_bf16 v[130:133], v[138:141], v[148:151], v[130:133]
	v_lshl_or_b32 v138, v143, 10, v198
	ds_read_b128 v[138:141], v138
	v_lshl_or_b32 v143, v143, 8, v204
	v_mfma_f32_16x16x32_bf16 v[134:137], v[144:147], v[148:151], v[134:137]
	ds_read_b128 v[144:147], v143
	ds_read_b128 v[148:151], v216
	v_bitop3_b32 v143, v232, 7, 32 bitop3:0xde
	s_waitcnt lgkmcnt(0)
	v_mfma_f32_16x16x32_bf16 v[130:133], v[138:141], v[148:151], v[130:133]
	v_lshl_or_b32 v138, v143, 10, v198
	v_lshl_or_b32 v143, v143, 8, v204
	ds_read_b128 v[138:141], v138
	v_mfma_f32_16x16x32_bf16 v[134:137], v[144:147], v[148:151], v[134:137]
	ds_read_b128 v[144:147], v143
	ds_read_b128 v[148:151], v213
	ds_write_b64 v212, v[2:3]
	s_waitcnt vmcnt(21)
	v_cvt_pk_bf16_f32 v2, v10, v11
	v_cvt_pk_bf16_f32 v3, v12, v13
	ds_write_b64 v211, v[2:3] offset:512
	s_waitcnt vmcnt(20)
	v_cvt_pk_bf16_f32 v2, v14, v15
	v_cvt_pk_bf16_f32 v3, v16, v17
	ds_write_b64 v210, v[2:3] offset:1024
	s_waitcnt vmcnt(19)
	v_cvt_pk_bf16_f32 v2, v22, v23
	v_cvt_pk_bf16_f32 v3, v24, v25
	ds_write_b64 v209, v[2:3] offset:1536
	s_waitcnt vmcnt(18)
	v_cvt_pk_bf16_f32 v2, v30, v31
	v_cvt_pk_bf16_f32 v3, v32, v33
	ds_write_b64 v208, v[2:3] offset:2048
	s_waitcnt vmcnt(17)
	v_cvt_pk_bf16_f32 v2, v38, v39
	v_cvt_pk_bf16_f32 v3, v40, v41
	ds_write_b64 v207, v[2:3] offset:2560
	s_waitcnt vmcnt(16)
	v_cvt_pk_bf16_f32 v2, v46, v47
	v_cvt_pk_bf16_f32 v3, v48, v49
	ds_write_b64 v206, v[2:3] offset:3072
	v_cvt_pk_bf16_f32 v2, v54, v55
	v_cvt_pk_bf16_f32 v3, v56, v57
	ds_write_b64 v205, v[2:3] offset:3584
	v_cvt_pk_bf16_f32 v2, v62, v63
	v_cvt_pk_bf16_f32 v3, v64, v65
	ds_write_b64 v231, v[2:3] offset:4096
	v_cvt_pk_bf16_f32 v2, v70, v71
	v_cvt_pk_bf16_f32 v3, v72, v73
	ds_write_b64 v230, v[2:3] offset:4608
	v_cvt_pk_bf16_f32 v2, v78, v79
	v_cvt_pk_bf16_f32 v3, v80, v81
	ds_write_b64 v229, v[2:3] offset:5120
	v_cvt_pk_bf16_f32 v2, v86, v87
	v_cvt_pk_bf16_f32 v3, v88, v89
	ds_write_b64 v228, v[2:3] offset:5632
	v_cvt_pk_bf16_f32 v2, v94, v95
	v_cvt_pk_bf16_f32 v3, v96, v97
	ds_write_b64 v227, v[2:3] offset:6144
	v_cvt_pk_bf16_f32 v2, v106, v107
	v_cvt_pk_bf16_f32 v3, v108, v109
	ds_write_b64 v226, v[2:3] offset:6656
	v_cvt_pk_bf16_f32 v2, v114, v115
	v_cvt_pk_bf16_f32 v3, v116, v117
	ds_write_b64 v225, v[2:3] offset:7168
	v_cvt_pk_bf16_f32 v2, v122, v123
	v_cvt_pk_bf16_f32 v3, v124, v125
	ds_write_b64 v224, v[2:3] offset:7680
	v_lshlrev_b32_e32 v2, 10, v142
	v_and_or_b32 v2, v2, s0, v203
	v_or_b32_e32 v3, 0x2000, v2
	buffer_load_dwordx4 v[10:13], v2, s[4:7], 0 offen nt
	buffer_load_dwordx4 v[14:17], v3, s[4:7], 0 offen nt
	v_or_b32_e32 v3, 0x4000, v2
	buffer_load_dwordx4 v[22:25], v3, s[4:7], 0 offen nt
	v_or_b32_e32 v3, 0x6000, v2
	buffer_load_dwordx4 v[30:33], v3, s[4:7], 0 offen nt
	v_or_b32_e32 v3, 0x8000, v2
	buffer_load_dwordx4 v[38:41], v3, s[4:7], 0 offen nt
	v_or_b32_e32 v3, 0xa000, v2
	buffer_load_dwordx4 v[46:49], v3, s[4:7], 0 offen nt
	v_or_b32_e32 v3, 0xc000, v2
	buffer_load_dwordx4 v[54:57], v3, s[4:7], 0 offen nt
	v_or_b32_e32 v3, 0xe000, v2
	buffer_load_dwordx4 v[62:65], v3, s[4:7], 0 offen nt
	v_or_b32_e32 v3, 0x10000, v2
	buffer_load_dwordx4 v[70:73], v3, s[4:7], 0 offen nt
	v_or_b32_e32 v3, 0x12000, v2
	buffer_load_dwordx4 v[78:81], v3, s[4:7], 0 offen nt
	v_or_b32_e32 v3, 0x14000, v2
	buffer_load_dwordx4 v[86:89], v3, s[4:7], 0 offen nt
	v_or_b32_e32 v3, 0x16000, v2
	buffer_load_dwordx4 v[94:97], v3, s[4:7], 0 offen nt
	v_or_b32_e32 v3, 0x18000, v2
	buffer_load_dwordx4 v[106:109], v3, s[4:7], 0 offen nt
	v_or_b32_e32 v3, 0x1a000, v2
	buffer_load_dwordx4 v[114:117], v3, s[4:7], 0 offen nt
	v_or_b32_e32 v3, 0x1c000, v2
	v_or_b32_e32 v2, 0x1e000, v2
	s_waitcnt lgkmcnt(14)
	v_mfma_f32_16x16x32_bf16 v[138:141], v[138:141], v[148:151], v[130:133]
	buffer_load_dwordx4 v[122:125], v3, s[4:7], 0 offen nt
	s_nop 1
	buffer_load_dwordx4 v[130:133], v2, s[4:7], 0 offen nt
	v_mfma_f32_16x16x32_bf16 v[134:137], v[144:147], v[148:151], v[134:137]
	v_lshlrev_b32_e32 v2, 3, v234
	v_and_b32_e32 v143, 56, v2
	v_lshl_or_b32 v2, v143, 10, v198
	v_lshl_or_b32 v152, v143, 8, v204
	ds_read_b128 v[2:5], v2
	ds_read_b128 v[144:147], v223
	ds_read_b128 v[148:151], v222
	ds_read_b128 v[152:155], v152
	v_or_b32_e32 v156, 1, v143
	v_lshl_or_b32 v157, v156, 10, v198
	s_waitcnt lgkmcnt(2)
	v_mfma_f32_16x16x32_bf16 v[2:5], v[2:5], v[144:147], v[138:141]
	s_waitcnt vmcnt(31)
	v_cvt_pk_bf16_f32 v6, v6, v7
	v_cvt_pk_bf16_f32 v7, v8, v9
	s_waitcnt lgkmcnt(0)
	v_mfma_f32_16x16x32_bf16 v[134:137], v[152:155], v[144:147], v[134:137]
	ds_read_b128 v[138:141], v157
	v_lshl_or_b32 v144, v156, 8, v204
	ds_read_b128 v[144:147], v144
	v_or_b32_e32 v156, 2, v143
	s_waitcnt lgkmcnt(1)
	v_mfma_f32_16x16x32_bf16 v[2:5], v[138:141], v[148:151], v[2:5]
	v_lshl_or_b32 v138, v156, 10, v198
	ds_read_b128 v[138:141], v138
	ds_read_b128 v[152:155], v221
	s_waitcnt lgkmcnt(2)
	v_mfma_f32_16x16x32_bf16 v[134:137], v[144:147], v[148:151], v[134:137]
	v_lshl_or_b32 v144, v156, 8, v204
	v_or_b32_e32 v156, 3, v143
	ds_read_b128 v[144:147], v144
	ds_read_b128 v[148:151], v219
	s_waitcnt lgkmcnt(2)
	v_mfma_f32_16x16x32_bf16 v[2:5], v[138:141], v[152:155], v[2:5]
	v_lshl_or_b32 v138, v156, 10, v198
	ds_read_b128 v[138:141], v138
	s_waitcnt lgkmcnt(2)
	v_mfma_f32_16x16x32_bf16 v[134:137], v[144:147], v[152:155], v[134:137]
	v_lshl_or_b32 v144, v156, 8, v204
	ds_read_b128 v[144:147], v144
	v_or_b32_e32 v152, 4, v143
	s_waitcnt lgkmcnt(1)
	v_mfma_f32_16x16x32_bf16 v[2:5], v[138:141], v[148:151], v[2:5]
	v_lshl_or_b32 v138, v152, 10, v198
	ds_read_b128 v[138:141], v138
	v_or_b32_e32 v156, 5, v143
	s_waitcnt lgkmcnt(1)
	v_mfma_f32_16x16x32_bf16 v[134:137], v[144:147], v[148:151], v[134:137]
	ds_read_b128 v[144:147], v218
	v_lshl_or_b32 v148, v152, 8, v204
	ds_read_b128 v[148:151], v148
	ds_read_b128 v[152:155], v217
	s_waitcnt lgkmcnt(2)
	v_mfma_f32_16x16x32_bf16 v[2:5], v[138:141], v[144:147], v[2:5]
	v_lshl_or_b32 v138, v156, 10, v198
	ds_read_b128 v[138:141], v138
	s_waitcnt lgkmcnt(2)
	v_mfma_f32_16x16x32_bf16 v[134:137], v[148:151], v[144:147], v[134:137]
	v_lshl_or_b32 v144, v156, 8, v204
	ds_read_b128 v[144:147], v144
	v_or_b32_e32 v148, 6, v143
	s_waitcnt lgkmcnt(1)
	v_mfma_f32_16x16x32_bf16 v[2:5], v[138:141], v[152:155], v[2:5]
	v_lshl_or_b32 v138, v148, 10, v198
	ds_read_b128 v[138:141], v138
	v_lshl_or_b32 v148, v148, 8, v204
	s_waitcnt lgkmcnt(1)
	v_mfma_f32_16x16x32_bf16 v[134:137], v[144:147], v[152:155], v[134:137]
	ds_read_b128 v[144:147], v216
	ds_read_b128 v[148:151], v148
	ds_read_b128 v[152:155], v213
	v_or_b32_e32 v143, 7, v143
	ds_write_b64 v212, v[6:7]
	s_waitcnt lgkmcnt(3)
	v_mfma_f32_16x16x32_bf16 v[2:5], v[138:141], v[144:147], v[2:5]
	v_lshl_or_b32 v138, v143, 10, v198
	v_lshl_or_b32 v143, v143, 8, v204
	s_waitcnt vmcnt(19)
	v_cvt_pk_bf16_f32 v6, v18, v19
	v_cvt_pk_bf16_f32 v7, v20, v21
	ds_read_b128 v[138:141], v138
	s_waitcnt lgkmcnt(3)
	v_mfma_f32_16x16x32_bf16 v[134:137], v[148:151], v[144:147], v[134:137]
	ds_read_b128 v[144:147], v143
	ds_write_b64 v211, v[6:7] offset:512
	s_waitcnt vmcnt(18)
	v_cvt_pk_bf16_f32 v6, v26, v27
	v_cvt_pk_bf16_f32 v7, v28, v29
	ds_write_b64 v210, v[6:7] offset:1024
	s_waitcnt vmcnt(17)
	v_cvt_pk_bf16_f32 v6, v34, v35
	v_cvt_pk_bf16_f32 v7, v36, v37
	ds_write_b64 v209, v[6:7] offset:1536
	s_waitcnt vmcnt(16)
	v_cvt_pk_bf16_f32 v6, v42, v43
	v_cvt_pk_bf16_f32 v7, v44, v45
	ds_write_b64 v208, v[6:7] offset:2048
	v_cvt_pk_bf16_f32 v6, v50, v51
	v_cvt_pk_bf16_f32 v7, v52, v53
	ds_write_b64 v207, v[6:7] offset:2560
	v_cvt_pk_bf16_f32 v6, v58, v59
	v_cvt_pk_bf16_f32 v7, v60, v61
	ds_write_b64 v206, v[6:7] offset:3072
	v_cvt_pk_bf16_f32 v6, v66, v67
	v_cvt_pk_bf16_f32 v7, v68, v69
	ds_write_b64 v205, v[6:7] offset:3584
	v_cvt_pk_bf16_f32 v6, v74, v75
	v_cvt_pk_bf16_f32 v7, v76, v77
	ds_write_b64 v231, v[6:7] offset:4096
	v_cvt_pk_bf16_f32 v6, v82, v83
	v_cvt_pk_bf16_f32 v7, v84, v85
	ds_write_b64 v230, v[6:7] offset:4608
	v_cvt_pk_bf16_f32 v6, v90, v91
	v_cvt_pk_bf16_f32 v7, v92, v93
	s_waitcnt lgkmcnt(9)
	v_mfma_f32_16x16x32_bf16 v[134:137], v[144:147], v[152:155], v[134:137]
	ds_write_b64 v229, v[6:7] offset:5120
	v_cvt_pk_bf16_f32 v6, v98, v99
	v_cvt_pk_bf16_f32 v7, v100, v101
	ds_write_b64 v228, v[6:7] offset:5632
	v_cvt_pk_bf16_f32 v6, v102, v103
	v_cvt_pk_bf16_f32 v7, v104, v105
	ds_write_b64 v227, v[6:7] offset:6144
	v_cvt_pk_bf16_f32 v6, v110, v111
	v_cvt_pk_bf16_f32 v7, v112, v113
	ds_write_b64 v226, v[6:7] offset:6656
	v_cvt_pk_bf16_f32 v6, v118, v119
	v_cvt_pk_bf16_f32 v7, v120, v121
	v_mfma_f32_16x16x32_bf16 v[2:5], v[138:141], v[152:155], v[2:5]
	ds_write_b64 v225, v[6:7] offset:7168
	v_cvt_pk_bf16_f32 v6, v126, v127
	v_cvt_pk_bf16_f32 v7, v128, v129
	ds_write_b64 v224, v[6:7] offset:7680
	v_add_u32_e32 v6, 48, v232
	v_and_b32_e32 v50, 56, v6
	v_lshl_or_b32 v6, v50, 10, v198
	v_lshl_or_b32 v34, v50, 8, v204
	ds_read_b128 v[6:9], v6
	ds_read_b128 v[18:21], v223
	ds_read_b128 v[26:29], v222
	ds_read_b128 v[34:37], v34
	v_or_b32_e32 v42, 1, v50
	v_lshl_or_b32 v43, v42, 10, v198
	s_waitcnt lgkmcnt(2)
	v_mfma_f32_16x16x32_bf16 v[2:5], v[6:9], v[18:21], v[2:5]
	ds_read_b128 v[6:9], v43
	v_or_b32_e32 v51, 2, v50
	s_waitcnt lgkmcnt(1)
	v_mfma_f32_16x16x32_bf16 v[18:21], v[34:37], v[18:21], v[134:137]
	v_lshl_or_b32 v34, v42, 8, v204
	ds_read_b128 v[34:37], v34
	s_waitcnt lgkmcnt(1)
	v_mfma_f32_16x16x32_bf16 v[2:5], v[6:9], v[26:29], v[2:5]
	v_lshl_or_b32 v6, v51, 10, v198
	ds_read_b128 v[6:9], v6
	ds_read_b128 v[42:45], v221
	s_waitcnt lgkmcnt(2)
	v_mfma_f32_16x16x32_bf16 v[18:21], v[34:37], v[26:29], v[18:21]
	v_lshl_or_b32 v26, v51, 8, v204
	v_or_b32_e32 v51, 3, v50
	ds_read_b128 v[26:29], v26
	ds_read_b128 v[34:37], v219
	s_waitcnt lgkmcnt(2)
	v_mfma_f32_16x16x32_bf16 v[2:5], v[6:9], v[42:45], v[2:5]
	v_lshl_or_b32 v6, v51, 10, v198
	ds_read_b128 v[6:9], v6
	s_waitcnt lgkmcnt(2)
	v_mfma_f32_16x16x32_bf16 v[18:21], v[26:29], v[42:45], v[18:21]
	v_lshl_or_b32 v26, v51, 8, v204
	ds_read_b128 v[26:29], v26
	v_or_b32_e32 v42, 4, v50
	s_waitcnt lgkmcnt(1)
	v_mfma_f32_16x16x32_bf16 v[2:5], v[6:9], v[34:37], v[2:5]
	v_lshl_or_b32 v6, v42, 10, v198
	ds_read_b128 v[6:9], v6
	v_or_b32_e32 v51, 5, v50
	s_waitcnt lgkmcnt(1)
	v_mfma_f32_16x16x32_bf16 v[18:21], v[26:29], v[34:37], v[18:21]
	ds_read_b128 v[26:29], v218
	v_lshl_or_b32 v34, v42, 8, v204
	ds_read_b128 v[34:37], v34
	ds_read_b128 v[42:45], v217
	s_waitcnt lgkmcnt(2)
	v_mfma_f32_16x16x32_bf16 v[2:5], v[6:9], v[26:29], v[2:5]
	v_lshl_or_b32 v6, v51, 10, v198
	ds_read_b128 v[6:9], v6
	s_waitcnt lgkmcnt(2)
	v_mfma_f32_16x16x32_bf16 v[18:21], v[34:37], v[26:29], v[18:21]
	v_lshl_or_b32 v26, v51, 8, v204
	ds_read_b128 v[26:29], v26
	v_or_b32_e32 v34, 6, v50
	s_waitcnt lgkmcnt(1)
	v_mfma_f32_16x16x32_bf16 v[2:5], v[6:9], v[42:45], v[2:5]
	v_lshl_or_b32 v6, v34, 10, v198
	ds_read_b128 v[6:9], v6
	v_lshl_or_b32 v34, v34, 8, v204
	s_waitcnt lgkmcnt(1)
	v_mfma_f32_16x16x32_bf16 v[18:21], v[26:29], v[42:45], v[18:21]
	ds_read_b128 v[26:29], v216
	ds_read_b128 v[34:37], v34
	ds_read_b128 v[42:45], v213
	v_or_b32_e32 v50, 7, v50
	s_waitcnt lgkmcnt(2)
	v_mfma_f32_16x16x32_bf16 v[2:5], v[6:9], v[26:29], v[2:5]
	v_lshl_or_b32 v6, v50, 10, v198
	ds_read_b128 v[6:9], v6
	s_waitcnt lgkmcnt(2)
	v_mfma_f32_16x16x32_bf16 v[18:21], v[34:37], v[26:29], v[18:21]
	v_lshl_or_b32 v26, v50, 8, v204
	ds_read_b128 v[26:29], v26
	s_waitcnt lgkmcnt(1)
	v_mfma_f32_16x16x32_bf16 v[34:37], v[6:9], v[42:45], v[2:5]
	v_and_b32_e32 v74, 7, v197
	v_lshrrev_b32_e32 v75, 3, v197
	v_lshlrev_b32_e32 v192, 13, v200
	v_lshlrev_b32_e32 v193, 11, v200
	v_lshl_add_u32 v203, v197, 2, v196
	v_lshl_or_b32 v192, v75, 8, v192
	v_lshl_or_b32 v193, v75, 6, v193
	v_add_u32_e32 v203, 0x24800, v203
	v_lshl_or_b32 v192, v201, 6, v192
	v_lshl_or_b32 v193, v74, 1, v193
	v_lshl_or_b32 v192, v74, 1, v192
	v_or_b32_e32 v193, 0x10000, v193
	v_cmp_gt_u32_e64 s[36:37], 16, v1
	v_cmp_eq_u32_e64 s[38:39], 1, v201
	ds_read2_b32 v[2:3], v203 offset1:16
	ds_read2_b32 v[4:5], v203 offset0:32 offset1:48
	ds_read2_b32 v[6:7], v203 offset0:64 offset1:80
	ds_read2_b32 v[8:9], v203 offset0:96 offset1:112
	ds_read2_b32 v[50:51], v203 offset0:128 offset1:144
	ds_read2_b32 v[52:53], v203 offset0:160 offset1:176
	ds_read2_b32 v[58:59], v203 offset0:192 offset1:208
	ds_read2_b32 v[60:61], v203 offset0:224 offset1:240
	v_mov_b32_e32 v146, 0
	v_mov_b32_e32 v147, 0
	v_mov_b32_e32 v150, 0
	v_mov_b32_e32 v151, 0
	v_mov_b32_e32 v154, 0
	v_mov_b32_e32 v155, 0
	v_mov_b32_e32 v158, 0
	v_mov_b32_e32 v159, 0
	v_mov_b32_e32 v162, 0
	v_mov_b32_e32 v163, 0
	v_mov_b32_e32 v166, 0
	v_mov_b32_e32 v167, 0
	v_mov_b32_e32 v170, 0
	v_mov_b32_e32 v171, 0
	v_mov_b32_e32 v174, 0
	v_mov_b32_e32 v175, 0
	v_mov_b32_e32 v178, 0
	v_mov_b32_e32 v179, 0
	v_mov_b32_e32 v182, 0
	v_mov_b32_e32 v183, 0
	v_mov_b32_e32 v186, 0
	v_mov_b32_e32 v187, 0
	v_mov_b32_e32 v190, 0
	v_mov_b32_e32 v191, 0
	v_mov_b32_e32 v234, 0
	v_mov_b32_e32 v235, 0
	v_mov_b32_e32 v238, 0
	v_mov_b32_e32 v239, 0
	v_mov_b32_e32 v242, 0
	v_mov_b32_e32 v243, 0
	v_mov_b32_e32 v246, 0
	v_mov_b32_e32 v247, 0
	ds_read_u16 v82, v192
	ds_read_u16 v83, v192 offset:16
	ds_read_u16 v84, v192 offset:32
	ds_read_u16 v85, v192 offset:48
	ds_read_u16 v90, v193
	ds_read_u16 v91, v193 offset:16
	ds_read_u16 v92, v193 offset:32
	ds_read_u16 v93, v193 offset:48
	ds_read_u16 v98, v192 offset:512
	ds_read_u16 v99, v192 offset:528
	ds_read_u16 v100, v192 offset:544
	ds_read_u16 v101, v192 offset:560
	ds_read_u16 v102, v193 offset:128
	ds_read_u16 v103, v193 offset:144
	ds_read_u16 v104, v193 offset:160
	ds_read_u16 v105, v193 offset:176
	s_waitcnt lgkmcnt(8)
	v_lshl_or_b32 v144, v83, 16, v82
	v_lshl_or_b32 v145, v85, 16, v84
	s_mov_b64 exec, s[36:37]
	v_lshl_or_b32 v146, v91, 16, v90
	v_lshl_or_b32 v147, v93, 16, v92
	s_mov_b64 exec, -1
	ds_read_u16 v82, v192 offset:1024
	ds_read_u16 v83, v192 offset:1040
	ds_read_u16 v84, v192 offset:1056
	ds_read_u16 v85, v192 offset:1072
	ds_read_u16 v90, v193 offset:256
	ds_read_u16 v91, v193 offset:272
	ds_read_u16 v92, v193 offset:288
	ds_read_u16 v93, v193 offset:304
	s_waitcnt lgkmcnt(8)
	v_lshl_or_b32 v148, v99, 16, v98
	v_lshl_or_b32 v149, v101, 16, v100
	s_mov_b64 exec, s[36:37]
	v_lshl_or_b32 v150, v103, 16, v102
	v_lshl_or_b32 v151, v105, 16, v104
	s_mov_b64 exec, -1
	ds_read_u16 v98, v192 offset:1536
	ds_read_u16 v99, v192 offset:1552
	ds_read_u16 v100, v192 offset:1568
	ds_read_u16 v101, v192 offset:1584
	ds_read_u16 v102, v193 offset:384
	ds_read_u16 v103, v193 offset:400
	ds_read_u16 v104, v193 offset:416
	ds_read_u16 v105, v193 offset:432
	s_waitcnt lgkmcnt(8)
	v_lshl_or_b32 v152, v83, 16, v82
	v_lshl_or_b32 v153, v85, 16, v84
	s_mov_b64 exec, s[36:37]
	v_lshl_or_b32 v154, v91, 16, v90
	v_lshl_or_b32 v155, v93, 16, v92
	s_mov_b64 exec, -1
	ds_read_u16 v82, v192 offset:2048
	ds_read_u16 v83, v192 offset:2064
	ds_read_u16 v84, v192 offset:2080
	ds_read_u16 v85, v192 offset:2096
	ds_read_u16 v90, v193 offset:512
	ds_read_u16 v91, v193 offset:528
	ds_read_u16 v92, v193 offset:544
	ds_read_u16 v93, v193 offset:560
	s_waitcnt lgkmcnt(8)
	v_lshl_or_b32 v156, v99, 16, v98
	v_lshl_or_b32 v157, v101, 16, v100
	s_mov_b64 exec, s[36:37]
	v_lshl_or_b32 v158, v103, 16, v102
	v_lshl_or_b32 v159, v105, 16, v104
	s_mov_b64 exec, -1
	ds_read_u16 v98, v192 offset:2560
	ds_read_u16 v99, v192 offset:2576
	ds_read_u16 v100, v192 offset:2592
	ds_read_u16 v101, v192 offset:2608
	ds_read_u16 v102, v193 offset:640
	ds_read_u16 v103, v193 offset:656
	ds_read_u16 v104, v193 offset:672
	ds_read_u16 v105, v193 offset:688
	s_waitcnt lgkmcnt(8)
	v_lshl_or_b32 v160, v83, 16, v82
	v_lshl_or_b32 v161, v85, 16, v84
	s_mov_b64 exec, s[36:37]
	v_lshl_or_b32 v162, v91, 16, v90
	v_lshl_or_b32 v163, v93, 16, v92
	s_mov_b64 exec, -1
	ds_read_u16 v82, v192 offset:3072
	ds_read_u16 v83, v192 offset:3088
	ds_read_u16 v84, v192 offset:3104
	ds_read_u16 v85, v192 offset:3120
	ds_read_u16 v90, v193 offset:768
	ds_read_u16 v91, v193 offset:784
	ds_read_u16 v92, v193 offset:800
	ds_read_u16 v93, v193 offset:816
	s_waitcnt lgkmcnt(8)
	v_lshl_or_b32 v164, v99, 16, v98
	v_lshl_or_b32 v165, v101, 16, v100
	s_mov_b64 exec, s[36:37]
	v_lshl_or_b32 v166, v103, 16, v102
	v_lshl_or_b32 v167, v105, 16, v104
	s_mov_b64 exec, -1
	ds_read_u16 v98, v192 offset:3584
	ds_read_u16 v99, v192 offset:3600
	ds_read_u16 v100, v192 offset:3616
	ds_read_u16 v101, v192 offset:3632
	ds_read_u16 v102, v193 offset:896
	ds_read_u16 v103, v193 offset:912
	ds_read_u16 v104, v193 offset:928
	ds_read_u16 v105, v193 offset:944
	s_waitcnt lgkmcnt(8)
	v_lshl_or_b32 v168, v83, 16, v82
	v_lshl_or_b32 v169, v85, 16, v84
	s_mov_b64 exec, s[36:37]
	v_lshl_or_b32 v170, v91, 16, v90
	v_lshl_or_b32 v171, v93, 16, v92
	s_mov_b64 exec, -1
	ds_read_u16 v82, v192 offset:4096
	ds_read_u16 v83, v192 offset:4112
	ds_read_u16 v84, v192 offset:4128
	ds_read_u16 v85, v192 offset:4144
	ds_read_u16 v90, v193 offset:1024
	ds_read_u16 v91, v193 offset:1040
	ds_read_u16 v92, v193 offset:1056
	ds_read_u16 v93, v193 offset:1072
	s_waitcnt lgkmcnt(8)
	v_lshl_or_b32 v172, v99, 16, v98
	v_lshl_or_b32 v173, v101, 16, v100
	s_mov_b64 exec, s[36:37]
	v_lshl_or_b32 v174, v103, 16, v102
	v_lshl_or_b32 v175, v105, 16, v104
	s_mov_b64 exec, -1
	ds_read_u16 v98, v192 offset:4608
	ds_read_u16 v99, v192 offset:4624
	ds_read_u16 v100, v192 offset:4640
	ds_read_u16 v101, v192 offset:4656
	ds_read_u16 v102, v193 offset:1152
	ds_read_u16 v103, v193 offset:1168
	ds_read_u16 v104, v193 offset:1184
	ds_read_u16 v105, v193 offset:1200
	s_waitcnt lgkmcnt(8)
	v_lshl_or_b32 v176, v83, 16, v82
	v_lshl_or_b32 v177, v85, 16, v84
	s_mov_b64 exec, s[36:37]
	v_lshl_or_b32 v178, v91, 16, v90
	v_lshl_or_b32 v179, v93, 16, v92
	s_mov_b64 exec, -1
	ds_read_u16 v82, v192 offset:5120
	ds_read_u16 v83, v192 offset:5136
	ds_read_u16 v84, v192 offset:5152
	ds_read_u16 v85, v192 offset:5168
	ds_read_u16 v90, v193 offset:1280
	ds_read_u16 v91, v193 offset:1296
	ds_read_u16 v92, v193 offset:1312
	ds_read_u16 v93, v193 offset:1328
	s_waitcnt lgkmcnt(8)
	v_lshl_or_b32 v180, v99, 16, v98
	v_lshl_or_b32 v181, v101, 16, v100
	s_mov_b64 exec, s[36:37]
	v_lshl_or_b32 v182, v103, 16, v102
	v_lshl_or_b32 v183, v105, 16, v104
	s_mov_b64 exec, -1
	ds_read_u16 v98, v192 offset:5632
	ds_read_u16 v99, v192 offset:5648
	ds_read_u16 v100, v192 offset:5664
	ds_read_u16 v101, v192 offset:5680
	ds_read_u16 v102, v193 offset:1408
	ds_read_u16 v103, v193 offset:1424
	ds_read_u16 v104, v193 offset:1440
	ds_read_u16 v105, v193 offset:1456
	s_waitcnt lgkmcnt(8)
	v_lshl_or_b32 v184, v83, 16, v82
	v_lshl_or_b32 v185, v85, 16, v84
	s_mov_b64 exec, s[36:37]
	v_lshl_or_b32 v186, v91, 16, v90
	v_lshl_or_b32 v187, v93, 16, v92
	s_mov_b64 exec, -1
	ds_read_u16 v82, v192 offset:6144
	ds_read_u16 v83, v192 offset:6160
	ds_read_u16 v84, v192 offset:6176
	ds_read_u16 v85, v192 offset:6192
	ds_read_u16 v90, v193 offset:1536
	ds_read_u16 v91, v193 offset:1552
	ds_read_u16 v92, v193 offset:1568
	ds_read_u16 v93, v193 offset:1584
	s_waitcnt lgkmcnt(8)
	v_lshl_or_b32 v188, v99, 16, v98
	v_lshl_or_b32 v189, v101, 16, v100
	s_mov_b64 exec, s[36:37]
	v_lshl_or_b32 v190, v103, 16, v102
	v_lshl_or_b32 v191, v105, 16, v104
	s_mov_b64 exec, -1
	ds_read_u16 v98, v192 offset:6656
	ds_read_u16 v99, v192 offset:6672
	ds_read_u16 v100, v192 offset:6688
	ds_read_u16 v101, v192 offset:6704
	ds_read_u16 v102, v193 offset:1664
	ds_read_u16 v103, v193 offset:1680
	ds_read_u16 v104, v193 offset:1696
	ds_read_u16 v105, v193 offset:1712
	s_waitcnt lgkmcnt(8)
	v_lshl_or_b32 v232, v83, 16, v82
	v_lshl_or_b32 v233, v85, 16, v84
	s_mov_b64 exec, s[36:37]
	v_lshl_or_b32 v234, v91, 16, v90
	v_lshl_or_b32 v235, v93, 16, v92
	s_mov_b64 exec, -1
	ds_read_u16 v82, v192 offset:7168
	ds_read_u16 v83, v192 offset:7184
	ds_read_u16 v84, v192 offset:7200
	ds_read_u16 v85, v192 offset:7216
	ds_read_u16 v90, v193 offset:1792
	ds_read_u16 v91, v193 offset:1808
	ds_read_u16 v92, v193 offset:1824
	ds_read_u16 v93, v193 offset:1840
	s_waitcnt lgkmcnt(8)
	v_lshl_or_b32 v236, v99, 16, v98
	v_lshl_or_b32 v237, v101, 16, v100
	s_mov_b64 exec, s[36:37]
	v_lshl_or_b32 v238, v103, 16, v102
	v_lshl_or_b32 v239, v105, 16, v104
	s_mov_b64 exec, -1
	ds_read_u16 v98, v192 offset:7680
	ds_read_u16 v99, v192 offset:7696
	ds_read_u16 v100, v192 offset:7712
	ds_read_u16 v101, v192 offset:7728
	ds_read_u16 v102, v193 offset:1920
	ds_read_u16 v103, v193 offset:1936
	ds_read_u16 v104, v193 offset:1952
	ds_read_u16 v105, v193 offset:1968
	s_waitcnt lgkmcnt(8)
	v_lshl_or_b32 v240, v83, 16, v82
	v_lshl_or_b32 v241, v85, 16, v84
	s_mov_b64 exec, s[36:37]
	v_lshl_or_b32 v242, v91, 16, v90
	v_lshl_or_b32 v243, v93, 16, v92
	s_mov_b64 exec, -1
	s_waitcnt lgkmcnt(0)
	v_lshl_or_b32 v244, v99, 16, v98
	v_lshl_or_b32 v245, v101, 16, v100
	s_mov_b64 exec, s[36:37]
	v_lshl_or_b32 v246, v103, 16, v102
	v_lshl_or_b32 v247, v105, 16, v104
	s_mov_b64 exec, -1
	s_waitcnt lgkmcnt(0)
	s_mov_b64 exec, s[38:39]
	v_cvt_pk_bf16_f32 v66, v2, v195
	v_cvt_pk_bf16_f32 v74, v3, v195
	v_lshlrev_b32_e32 v67, 16, v66
	v_lshlrev_b32_e32 v75, 16, v74
	v_sub_f32_e32 v2, v2, v67
	v_sub_f32_e32 v3, v3, v75
	v_cvt_pk_bf16_f32 v68, v2, v195
	v_cvt_pk_bf16_f32 v76, v3, v195
	v_lshlrev_b32_e32 v69, 16, v68
	v_lshlrev_b32_e32 v77, 16, v76
	v_sub_f32_e32 v2, v2, v69
	v_sub_f32_e32 v3, v3, v77
	v_cvt_pk_bf16_f32 v147, v2, v195
	v_cvt_pk_bf16_f32 v151, v3, v195
	v_cvt_pk_bf16_f32 v146, v67, v69
	v_cvt_pk_bf16_f32 v150, v75, v77
	v_cvt_pk_bf16_f32 v66, v4, v195
	v_cvt_pk_bf16_f32 v74, v5, v195
	v_lshlrev_b32_e32 v67, 16, v66
	v_lshlrev_b32_e32 v75, 16, v74
	v_sub_f32_e32 v4, v4, v67
	v_sub_f32_e32 v5, v5, v75
	v_cvt_pk_bf16_f32 v68, v4, v195
	v_cvt_pk_bf16_f32 v76, v5, v195
	v_lshlrev_b32_e32 v69, 16, v68
	v_lshlrev_b32_e32 v77, 16, v76
	v_sub_f32_e32 v4, v4, v69
	v_sub_f32_e32 v5, v5, v77
	v_cvt_pk_bf16_f32 v155, v4, v195
	v_cvt_pk_bf16_f32 v159, v5, v195
	v_cvt_pk_bf16_f32 v154, v67, v69
	v_cvt_pk_bf16_f32 v158, v75, v77
	v_cvt_pk_bf16_f32 v66, v6, v195
	v_cvt_pk_bf16_f32 v74, v7, v195
	v_lshlrev_b32_e32 v67, 16, v66
	v_lshlrev_b32_e32 v75, 16, v74
	v_sub_f32_e32 v6, v6, v67
	v_sub_f32_e32 v7, v7, v75
	v_cvt_pk_bf16_f32 v68, v6, v195
	v_cvt_pk_bf16_f32 v76, v7, v195
	v_lshlrev_b32_e32 v69, 16, v68
	v_lshlrev_b32_e32 v77, 16, v76
	v_sub_f32_e32 v6, v6, v69
	v_sub_f32_e32 v7, v7, v77
	v_cvt_pk_bf16_f32 v163, v6, v195
	v_cvt_pk_bf16_f32 v167, v7, v195
	v_cvt_pk_bf16_f32 v162, v67, v69
	v_cvt_pk_bf16_f32 v166, v75, v77
	v_cvt_pk_bf16_f32 v66, v8, v195
	v_cvt_pk_bf16_f32 v74, v9, v195
	v_lshlrev_b32_e32 v67, 16, v66
	v_lshlrev_b32_e32 v75, 16, v74
	v_sub_f32_e32 v8, v8, v67
	v_sub_f32_e32 v9, v9, v75
	v_cvt_pk_bf16_f32 v68, v8, v195
	v_cvt_pk_bf16_f32 v76, v9, v195
	v_lshlrev_b32_e32 v69, 16, v68
	v_lshlrev_b32_e32 v77, 16, v76
	v_sub_f32_e32 v8, v8, v69
	v_sub_f32_e32 v9, v9, v77
	v_cvt_pk_bf16_f32 v171, v8, v195
	v_cvt_pk_bf16_f32 v175, v9, v195
	v_cvt_pk_bf16_f32 v170, v67, v69
	v_cvt_pk_bf16_f32 v174, v75, v77
	v_cvt_pk_bf16_f32 v66, v50, v195
	v_cvt_pk_bf16_f32 v74, v51, v195
	v_lshlrev_b32_e32 v67, 16, v66
	v_lshlrev_b32_e32 v75, 16, v74
	v_sub_f32_e32 v50, v50, v67
	v_sub_f32_e32 v51, v51, v75
	v_cvt_pk_bf16_f32 v68, v50, v195
	v_cvt_pk_bf16_f32 v76, v51, v195
	v_lshlrev_b32_e32 v69, 16, v68
	v_lshlrev_b32_e32 v77, 16, v76
	v_sub_f32_e32 v50, v50, v69
	v_sub_f32_e32 v51, v51, v77
	v_cvt_pk_bf16_f32 v179, v50, v195
	v_cvt_pk_bf16_f32 v183, v51, v195
	v_cvt_pk_bf16_f32 v178, v67, v69
	v_cvt_pk_bf16_f32 v182, v75, v77
	v_cvt_pk_bf16_f32 v66, v52, v195
	v_cvt_pk_bf16_f32 v74, v53, v195
	v_lshlrev_b32_e32 v67, 16, v66
	v_lshlrev_b32_e32 v75, 16, v74
	v_sub_f32_e32 v52, v52, v67
	v_sub_f32_e32 v53, v53, v75
	v_cvt_pk_bf16_f32 v68, v52, v195
	v_cvt_pk_bf16_f32 v76, v53, v195
	v_lshlrev_b32_e32 v69, 16, v68
	v_lshlrev_b32_e32 v77, 16, v76
	v_sub_f32_e32 v52, v52, v69
	v_sub_f32_e32 v53, v53, v77
	v_cvt_pk_bf16_f32 v187, v52, v195
	v_cvt_pk_bf16_f32 v191, v53, v195
	v_cvt_pk_bf16_f32 v186, v67, v69
	v_cvt_pk_bf16_f32 v190, v75, v77
	v_cvt_pk_bf16_f32 v66, v58, v195
	v_cvt_pk_bf16_f32 v74, v59, v195
	v_lshlrev_b32_e32 v67, 16, v66
	v_lshlrev_b32_e32 v75, 16, v74
	v_sub_f32_e32 v58, v58, v67
	v_sub_f32_e32 v59, v59, v75
	v_cvt_pk_bf16_f32 v68, v58, v195
	v_cvt_pk_bf16_f32 v76, v59, v195
	v_lshlrev_b32_e32 v69, 16, v68
	v_lshlrev_b32_e32 v77, 16, v76
	v_sub_f32_e32 v58, v58, v69
	v_sub_f32_e32 v59, v59, v77
	v_cvt_pk_bf16_f32 v235, v58, v195
	v_cvt_pk_bf16_f32 v239, v59, v195
	v_cvt_pk_bf16_f32 v234, v67, v69
	v_cvt_pk_bf16_f32 v238, v75, v77
	v_cvt_pk_bf16_f32 v66, v60, v195
	v_cvt_pk_bf16_f32 v74, v61, v195
	v_lshlrev_b32_e32 v67, 16, v66
	v_lshlrev_b32_e32 v75, 16, v74
	v_sub_f32_e32 v60, v60, v67
	v_sub_f32_e32 v61, v61, v75
	v_cvt_pk_bf16_f32 v68, v60, v195
	v_cvt_pk_bf16_f32 v76, v61, v195
	v_lshlrev_b32_e32 v69, 16, v68
	v_lshlrev_b32_e32 v77, 16, v76
	v_sub_f32_e32 v60, v60, v69
	v_sub_f32_e32 v61, v61, v77
	v_cvt_pk_bf16_f32 v243, v60, v195
	v_cvt_pk_bf16_f32 v247, v61, v195
	v_cvt_pk_bf16_f32 v242, v67, v69
	v_cvt_pk_bf16_f32 v246, v75, v77
	s_mov_b64 exec, -1
	s_movk_i32 s44, 0x210
	v_and_b32_e32 v192, 48, v0
	v_lshrrev_b32_e32 v193, 5, v1
	v_mad_u32_u24 v214, v197, s44, v199
	v_mad_u32_u24 v215, v193, s44, v199
	v_add_u32_e32 v214, v214, v192
	v_and_b32_e32 v192, 0x1f0, v194
	v_add_u32_e32 v215, v215, v192
	s_and_b32 s44, s2, 7
	s_lshl_b32 s44, s44, 22
	s_lshl_b32 s45, s3, 17
	s_add_i32 s44, s44, s45
	v_lshlrev_b32_e32 v220, 13, v193
	v_or3_b32 v220, s44, v220, v196
	v_add_u32_e32 v220, v220, v192
	v_or_b32_e32 v203, 0x24800, v198
	s_mov_b32 s12, 0
	s_mov_b32 s11, 0x20000
	s_brev_b32 s10, 8
	s_and_b32 s9, s9, 0xffff
	v_lshlrev_b32_e32 v192, 3, v142
	v_and_b32_e32 v192, 56, v192
	v_lshl_or_b32 v193, v192, 8, v204
	v_lshl_or_b32 v192, v192, 10, v198
	s_nop 4
	v_mfma_f32_16x16x32_bf16 v[2:5], v[26:29], v[42:45], v[18:21]
	s_nop 1
	ds_read_b128 v[58:61], v192
	ds_read_b128 v[110:113], v193
	ds_read_b128 v[50:53], v192 offset:1024
	ds_read_b128 v[118:121], v193 offset:256
	ds_read_b128 v[66:69], v192 offset:2048
	ds_read_b128 v[126:129], v193 offset:512
	ds_read_b128 v[74:77], v192 offset:3072
	ds_read_b128 v[134:137], v193 offset:768
	ds_read_b128 v[82:85], v192 offset:4096
	ds_read_b128 v[138:141], v193 offset:1024
	ds_read_b128 v[90:93], v192 offset:5120
	ds_read_b128 v[18:21], v193 offset:1280
	ds_read_b128 v[98:101], v192 offset:6144
	ds_read_b128 v[26:29], v193 offset:1536
	ds_read_b128 v[102:105], v192 offset:7168
	ds_read_b128 v[42:45], v193 offset:1792
	s_waitcnt vmcnt(15)
	v_cvt_pk_bf16_f32 v6, v10, v11
	v_cvt_pk_bf16_f32 v7, v12, v13
	ds_write_b64 v212, v[6:7]
	s_waitcnt vmcnt(14)
	v_cvt_pk_bf16_f32 v6, v14, v15
	v_cvt_pk_bf16_f32 v7, v16, v17
	ds_write_b64 v211, v[6:7] offset:512
	s_waitcnt vmcnt(13)
	v_cvt_pk_bf16_f32 v6, v22, v23
	v_cvt_pk_bf16_f32 v7, v24, v25
	ds_write_b64 v210, v[6:7] offset:1024
	s_waitcnt vmcnt(12)
	v_cvt_pk_bf16_f32 v6, v30, v31
	v_cvt_pk_bf16_f32 v7, v32, v33
	ds_write_b64 v209, v[6:7] offset:1536
	s_waitcnt vmcnt(11)
	v_cvt_pk_bf16_f32 v6, v38, v39
	v_cvt_pk_bf16_f32 v7, v40, v41
	ds_write_b64 v208, v[6:7] offset:2048
	s_waitcnt vmcnt(10)
	v_cvt_pk_bf16_f32 v6, v46, v47
	v_cvt_pk_bf16_f32 v7, v48, v49
	ds_write_b64 v207, v[6:7] offset:2560
	s_waitcnt vmcnt(9)
	v_cvt_pk_bf16_f32 v6, v54, v55
	v_cvt_pk_bf16_f32 v7, v56, v57
	ds_write_b64 v206, v[6:7] offset:3072
	s_waitcnt vmcnt(8)
	v_cvt_pk_bf16_f32 v6, v62, v63
	v_cvt_pk_bf16_f32 v7, v64, v65
	ds_write_b64 v205, v[6:7] offset:3584
	s_waitcnt vmcnt(7)
	v_cvt_pk_bf16_f32 v6, v70, v71
	v_cvt_pk_bf16_f32 v7, v72, v73
	ds_write_b64 v231, v[6:7] offset:4096
	s_waitcnt vmcnt(6)
	v_cvt_pk_bf16_f32 v6, v78, v79
	v_cvt_pk_bf16_f32 v7, v80, v81
	ds_write_b64 v230, v[6:7] offset:4608
	s_waitcnt vmcnt(5)
	v_cvt_pk_bf16_f32 v6, v86, v87
	v_cvt_pk_bf16_f32 v7, v88, v89
	ds_write_b64 v229, v[6:7] offset:5120
	s_waitcnt vmcnt(4)
	v_cvt_pk_bf16_f32 v6, v94, v95
	v_cvt_pk_bf16_f32 v7, v96, v97
	ds_write_b64 v228, v[6:7] offset:5632
	s_waitcnt vmcnt(3)
	v_cvt_pk_bf16_f32 v6, v106, v107
	v_cvt_pk_bf16_f32 v7, v108, v109
	ds_write_b64 v227, v[6:7] offset:6144
	s_waitcnt vmcnt(2)
	v_cvt_pk_bf16_f32 v6, v114, v115
	v_cvt_pk_bf16_f32 v7, v116, v117
	ds_write_b64 v226, v[6:7] offset:6656
	s_waitcnt vmcnt(1)
	v_cvt_pk_bf16_f32 v6, v122, v123
	v_cvt_pk_bf16_f32 v7, v124, v125
	ds_write_b64 v225, v[6:7] offset:7168
	s_waitcnt vmcnt(0)
	v_cvt_pk_bf16_f32 v6, v130, v131
	v_cvt_pk_bf16_f32 v7, v132, v133
	ds_write_b64 v224, v[6:7] offset:7680
	ds_read_b128 v[54:57], v223
	ds_read_b128 v[62:65], v222
	ds_read_b128 v[10:13], v221
	ds_read_b128 v[14:17], v219
	ds_read_b128 v[22:25], v218
	ds_read_b128 v[30:33], v217
	ds_read_b128 v[38:41], v216
	ds_read_b128 v[46:49], v213
	s_waitcnt lgkmcnt(7)
	v_mfma_f32_16x16x32_bf16 v[34:37], v[58:61], v[54:57], v[34:37]
	v_mfma_f32_16x16x32_bf16 v[2:5], v[110:113], v[54:57], v[2:5]
	s_waitcnt lgkmcnt(6)
	v_mfma_f32_16x16x32_bf16 v[34:37], v[50:53], v[62:65], v[34:37]
	v_mfma_f32_16x16x32_bf16 v[2:5], v[118:121], v[62:65], v[2:5]
	s_waitcnt lgkmcnt(5)
	v_mfma_f32_16x16x32_bf16 v[34:37], v[66:69], v[10:13], v[34:37]
	v_mfma_f32_16x16x32_bf16 v[2:5], v[126:129], v[10:13], v[2:5]
	s_waitcnt lgkmcnt(4)
	v_mfma_f32_16x16x32_bf16 v[34:37], v[74:77], v[14:17], v[34:37]
	v_mfma_f32_16x16x32_bf16 v[2:5], v[134:137], v[14:17], v[2:5]
	s_waitcnt lgkmcnt(3)
	v_mfma_f32_16x16x32_bf16 v[34:37], v[82:85], v[22:25], v[34:37]
	v_mfma_f32_16x16x32_bf16 v[2:5], v[138:141], v[22:25], v[2:5]
	s_waitcnt lgkmcnt(2)
	v_mfma_f32_16x16x32_bf16 v[34:37], v[90:93], v[30:33], v[34:37]
	v_mfma_f32_16x16x32_bf16 v[2:5], v[18:21], v[30:33], v[2:5]
	s_waitcnt lgkmcnt(1)
	v_mfma_f32_16x16x32_bf16 v[34:37], v[98:101], v[38:41], v[34:37]
	v_mfma_f32_16x16x32_bf16 v[2:5], v[26:29], v[38:41], v[2:5]
	s_waitcnt lgkmcnt(0)
	v_mfma_f32_16x16x32_bf16 v[56:59], v[102:105], v[46:49], v[34:37]
	v_mfma_f32_16x16x32_bf16 v[60:63], v[42:45], v[46:49], v[2:5]
	v_add_u32_e32 v76, 0x24800, v196
	s_waitcnt lgkmcnt(0)
	v_cmp_gt_u32_e64 s[0:1], 16, v1
	v_cmp_lt_u32_e32 vcc, 15, v1
	s_waitcnt lgkmcnt(0)
	s_nop 2
	v_max_f32_e32 v2, v59, v59
	v_max_f32_e32 v3, v58, v58
	s_waitcnt lgkmcnt(0)
	v_max_f32_e32 v2, v3, v2
	s_nop 0
	s_nop 0
	s_nop 0
	s_waitcnt lgkmcnt(0)
	s_nop 0
	s_nop 0
	s_and_saveexec_b64 s[4:5], vcc
	s_xor_b64 s[4:5], exec, s[4:5]
	s_or_saveexec_b64 s[4:5], s[4:5]
	v_max3_f32 v53, v56, v57, v2
	s_xor_b64 exec, exec, s[4:5]
	v_max_f32_e32 v2, v61, v61
	v_max_f32_e32 v3, v60, v60
	v_max_f32_e32 v2, v3, v2
	v_max_f32_e32 v3, v63, v63
	v_max_f32_e32 v4, v62, v62
	v_max_f32_e32 v3, v4, v3
	v_max3_f32 v53, v53, v2, v3
	s_or_b64 exec, exec, s[4:5]
	v_cmp_eq_u32_e64 s[4:5], 1, v201
	v_max_f32_e32 v53, v53, v53
	v_mov_b32_e32 v68, v53
	s_nop 1
	v_permlane16_swap_b32_e32 v53, v68
	v_max_f32_e32 v68, v53, v68
	v_mov_b32_e32 v55, v68
	s_nop 1
	v_permlane32_swap_b32_e32 v68, v55
	v_max_f32_e32 v68, v68, v55
	v_sub_f32_e32 v55, v56, v68
	v_mul_f32_e32 v55, 0x3fb8aa3b, v55
	v_exp_f32_e32 v70, v55
	v_sub_f32_e32 v55, v57, v68
	v_sub_f32_e32 v57, v59, v68
	v_mul_f32_e32 v57, 0x3fb8aa3b, v57
	v_mul_f32_e32 v55, 0x3fb8aa3b, v55
	v_exp_f32_e32 v59, v57
	v_sub_f32_e32 v57, v60, v68
	v_exp_f32_e32 v71, v55
	v_sub_f32_e32 v55, v58, v68
	v_mul_f32_e32 v57, 0x3fb8aa3b, v57
	v_sub_f32_e32 v58, v61, v68
	v_exp_f32_e32 v57, v57
	v_mul_f32_e32 v58, 0x3fb8aa3b, v58
	v_exp_f32_e32 v58, v58
	v_mul_f32_e32 v55, 0x3fb8aa3b, v55
	v_exp_f32_e32 v72, v55
	v_cndmask_b32_e64 v60, 0, v57, s[0:1]
	v_sub_f32_e32 v57, v62, v68
	v_add_f32_e32 v56, 0, v70
	v_cndmask_b32_e64 v61, 0, v58, s[0:1]
	v_mul_f32_e32 v57, 0x3fb8aa3b, v57
	v_sub_f32_e32 v58, v63, v68
	v_add_f32_e32 v56, v56, v71
	v_exp_f32_e32 v57, v57
	v_mul_f32_e32 v58, 0x3fb8aa3b, v58
	v_add_f32_e32 v56, v56, v72
	v_exp_f32_e32 v58, v58
	v_add_f32_e32 v56, v56, v59
	v_add_f32_e32 v56, v56, v60
	v_add_f32_e32 v56, v56, v61
	v_cndmask_b32_e64 v62, 0, v57, s[0:1]
	v_add_f32_e32 v56, v56, v62
	v_cndmask_b32_e64 v63, 0, v58, s[0:1]
	v_add_f32_e32 v57, v56, v63
	v_mov_b32_e32 v58, v57
	s_nop 1
	v_permlane16_swap_b32_e32 v57, v58
	v_add_f32_e32 v58, v57, v58
	v_mov_b32_e32 v68, v58
	s_nop 1
	v_permlane32_swap_b32_e32 v58, v68
	v_add_f32_e32 v68, v58, v68
	v_div_scale_f32 v69, s[6:7], v68, v68, 1.0
	v_rcp_f32_e32 v73, v69
	s_nop 0
	v_fma_f32 v75, -v69, v73, 1.0
	v_fmac_f32_e32 v73, v75, v73
	v_div_scale_f32 v75, vcc, 1.0, v68, 1.0
	v_mul_f32_e32 v92, v75, v73
	v_fma_f32 v93, -v69, v92, v75
	v_fmac_f32_e32 v92, v93, v73
	v_fma_f32 v69, -v69, v92, v75
	v_div_fmas_f32 v69, v69, v73, v92
	v_div_fixup_f32 v68, v69, v68, 1.0
	v_mul_f32_e32 v69, v68, v70
	v_mov_b32_e32 v75, 0xbb23d70a
	v_mov_b32_e32 v73, 0x3b23d70a
	v_fmaak_f32 v92, v68, v70, 0xbb23d70a
	v_fmaak_f32 v70, v68, v70, 0x3b23d70a
	v_cmp_lt_f32_e32 vcc, v69, v75
	v_fmaak_f32 v93, v68, v60, 0xbb23d70a
	s_nop 0
	v_cndmask_b32_e32 v70, 0, v70, vcc
	v_cmp_gt_f32_e32 vcc, v69, v73
	s_nop 1
	v_cndmask_b32_e32 v69, v70, v92, vcc
	v_mul_f32_e32 v92, v68, v60
	v_fmaak_f32 v60, v68, v60, 0x3b23d70a
	v_cmp_lt_f32_e32 vcc, v92, v75
	v_max_f32_e32 v70, 0xf149f2ca, v69
	s_nop 0
	v_cndmask_b32_e32 v60, 0, v60, vcc
	v_cmp_gt_f32_e32 vcc, v92, v73
	s_nop 1
	v_cndmask_b32_e32 v92, v60, v93, vcc
	v_max_f32_e32 v60, v70, v92
	v_cndmask_b32_e64 v60, v70, v60, s[0:1]
	v_mul_f32_e32 v70, v68, v71
	v_fmaak_f32 v93, v68, v71, 0xbb23d70a
	v_fmaak_f32 v71, v68, v71, 0x3b23d70a
	v_cmp_lt_f32_e32 vcc, v70, v75
	s_nop 1
	v_cndmask_b32_e32 v71, 0, v71, vcc
	v_cmp_gt_f32_e32 vcc, v70, v73
	s_nop 1
	v_cndmask_b32_e32 v70, v71, v93, vcc
	v_mul_f32_e32 v71, v68, v61
	v_fmaak_f32 v93, v68, v61, 0xbb23d70a
	v_fmaak_f32 v61, v68, v61, 0x3b23d70a
	v_cmp_lt_f32_e32 vcc, v71, v75
	v_max_f32_e32 v60, v60, v70
	s_nop 0
	v_cndmask_b32_e32 v61, 0, v61, vcc
	v_cmp_gt_f32_e32 vcc, v71, v73
	s_nop 1
	v_cndmask_b32_e32 v71, v61, v93, vcc
	v_max_f32_e32 v61, v60, v71
	v_cndmask_b32_e64 v60, v60, v61, s[0:1]
	v_mul_f32_e32 v61, v68, v72
	v_fmaak_f32 v93, v68, v72, 0xbb23d70a
	v_fmaak_f32 v72, v68, v72, 0x3b23d70a
	v_cmp_lt_f32_e32 vcc, v61, v75
	s_nop 1
	v_cndmask_b32_e32 v72, 0, v72, vcc
	v_cmp_gt_f32_e32 vcc, v61, v73
	v_mul_f32_e32 v61, v68, v62
	s_nop 0
	v_cndmask_b32_e32 v72, v72, v93, vcc
	v_fmaak_f32 v93, v68, v62, 0xbb23d70a
	v_fmaak_f32 v62, v68, v62, 0x3b23d70a
	v_cmp_lt_f32_e32 vcc, v61, v75
	v_max_f32_e32 v60, v60, v72
	s_nop 0
	v_cndmask_b32_e32 v62, 0, v62, vcc
	v_cmp_gt_f32_e32 vcc, v61, v73
	s_nop 1
	v_cndmask_b32_e32 v62, v62, v93, vcc
	v_max_f32_e32 v61, v60, v62
	v_cndmask_b32_e64 v60, v60, v61, s[0:1]
	v_mul_f32_e32 v61, v68, v59
	v_fmaak_f32 v93, v68, v59, 0xbb23d70a
	v_fmaak_f32 v59, v68, v59, 0x3b23d70a
	v_cmp_lt_f32_e32 vcc, v61, v75
	s_nop 1
	v_cndmask_b32_e32 v59, 0, v59, vcc
	v_cmp_gt_f32_e32 vcc, v61, v73
	s_nop 1
	v_cndmask_b32_e32 v93, v59, v93, vcc
	v_max_f32_e32 v59, v60, v93
	v_mul_f32_e32 v60, v68, v63
	v_cmp_gt_f32_e32 vcc, v60, v73
	v_fmac_f32_e32 v73, v68, v63
	v_cmp_lt_f32_e64 s[6:7], v60, v75
	v_fmac_f32_e32 v75, v68, v63
	s_nop 0
	v_cndmask_b32_e64 v60, 0, v73, s[6:7]
	v_cndmask_b32_e32 v63, v60, v75, vcc
	v_max_f32_e32 v60, v59, v63
	v_cndmask_b32_e64 v60, v59, v60, s[0:1]
	v_mov_b32_e32 v61, v60
	s_nop 1
	v_permlane16_swap_b32_e32 v60, v61
	v_max_f32_e32 v61, v60, v61
	v_mov_b32_e32 v74, v61
	s_nop 1
	v_permlane32_swap_b32_e32 v61, v74
	v_max_f32_e32 v74, v61, v74
	v_sub_f32_e32 v61, v69, v74
	v_mul_f32_e32 v61, 0x3fb8aa3b, v61
	v_exp_f32_e32 v69, v61
	v_sub_f32_e32 v61, v92, v74
	v_mul_f32_e32 v61, 0x3fb8aa3b, v61
	v_exp_f32_e32 v75, v61
	v_sub_f32_e32 v70, v70, v74
	v_sub_f32_e32 v71, v71, v74
	v_mul_f32_e32 v70, 0x3fb8aa3b, v70
	v_mul_f32_e32 v71, 0x3fb8aa3b, v71
	v_exp_f32_e32 v70, v70
	v_exp_f32_e32 v71, v71
	v_sub_f32_e32 v72, v72, v74
	v_sub_f32_e32 v62, v62, v74
	v_mul_f32_e32 v72, 0x3fb8aa3b, v72
	v_mul_f32_e32 v62, 0x3fb8aa3b, v62
	v_add_f32_e32 v73, 0, v69
	v_cndmask_b32_e64 v75, 0, v75, s[0:1]
	v_exp_f32_e32 v72, v72
	v_exp_f32_e32 v62, v62
	v_sub_f32_e32 v84, v93, v74
	v_sub_f32_e32 v63, v63, v74
	v_add_f32_e32 v73, v73, v75
	v_mul_f32_e32 v84, 0x3fb8aa3b, v84
	v_mul_f32_e32 v63, 0x3fb8aa3b, v63
	v_add_f32_e32 v73, v73, v70
	v_cndmask_b32_e64 v71, 0, v71, s[0:1]
	v_exp_f32_e32 v84, v84
	v_exp_f32_e32 v63, v63
	v_add_f32_e32 v73, v73, v71
	v_add_f32_e32 v73, v73, v72
	v_cndmask_b32_e64 v74, 0, v62, s[0:1]
	v_add_f32_e32 v62, v73, v74
	v_add_f32_e32 v62, v62, v84
	v_cndmask_b32_e64 v73, 0, v63, s[0:1]
	v_add_f32_e32 v85, v62, v73
	v_mov_b32_e32 v66, v85
	s_nop 1
	v_permlane16_swap_b32_e32 v85, v66
	v_add_f32_e32 v66, v85, v66
	v_mov_b32_e32 v67, v66
	s_nop 1
	v_permlane32_swap_b32_e32 v66, v67
	v_add_f32_e32 v66, v66, v67
	v_div_scale_f32 v67, s[6:7], v66, v66, 1.0
	v_rcp_f32_e32 v78, v67
	s_nop 0
	v_fma_f32 v68, -v67, v78, 1.0
	v_fmac_f32_e32 v78, v68, v78
	v_div_scale_f32 v68, vcc, 1.0, v66, 1.0
	v_mul_f32_e32 v77, v68, v78
	v_fma_f32 v79, -v67, v77, v68
	v_fmac_f32_e32 v77, v79, v78
	v_fma_f32 v67, -v67, v77, v68
	v_div_fmas_f32 v67, v67, v78, v77
	v_div_fixup_f32 v66, v67, v66, 1.0
	v_mov_b32_e32 v67, 0xbd4ccccd
	v_fmaak_f32 v68, v66, v69, 0xbd4ccccd
	v_fmaak_f32 v69, v66, v70, 0xbd4ccccd
	v_fmaak_f32 v70, v66, v72, 0xbd4ccccd
	v_fmaak_f32 v75, v66, v75, 0xbd4ccccd
	v_fmaak_f32 v71, v66, v71, 0xbd4ccccd
	v_fmaak_f32 v74, v66, v74, 0xbd4ccccd
	v_mul_f32_e32 v70, 0x4038aa3b, v70
	v_fmaak_f32 v72, v66, v84, 0xbd4ccccd
	v_mul_f32_e32 v75, 0x4038aa3b, v75
	v_mul_f32_e32 v71, 0x4038aa3b, v71
	v_mul_f32_e32 v74, 0x4038aa3b, v74
	v_fmac_f32_e32 v67, v66, v73
	v_mul_f32_e32 v68, 0x4038aa3b, v68
	v_mul_f32_e32 v69, 0x4038aa3b, v69
	v_mul_f32_e32 v72, 0x4038aa3b, v72
	v_cndmask_b32_e64 v75, 0, v75, s[0:1]
	v_cndmask_b32_e64 v71, 0, v71, s[0:1]
	v_cndmask_b32_e64 v74, 0, v74, s[0:1]
	v_mul_f32_e32 v66, 0x4038aa3b, v67
	v_cvt_pk_bf16_f32 v67, v70, v72
	v_add_u32_e32 v70, v76, v198
	v_cndmask_b32_e64 v73, 0, v66, s[0:1]
	v_cndmask_b32_e64 v74, v74, 1.0, s[4:5]
	v_cndmask_b32_e64 v75, v75, 1.0, s[4:5]
	v_cndmask_b32_e64 v71, v71, 1.0, s[4:5]
	v_cvt_pk_bf16_f32 v66, v68, v69
	v_cvt_pk_bf16_f32 v68, v75, v71
	v_cvt_pk_bf16_f32 v69, v74, v73
	ds_write_b128 v70, v[66:69]
	s_waitcnt lgkmcnt(0)
	s_barrier
.LBB0_3:
	ds_read_b128 v[70:73], v203
	v_add_u32_e32 v132, s12, v220
	s_add_i32 s12, s12, 0x2000000
	v_add_u32_e32 v203, 0x400, v203
	s_cmp_eq_u32 s12, 0x10000000
	s_waitcnt lgkmcnt(0)
	v_mfma_f32_16x16x32_bf16 v[66:69], v[144:147], v[70:73], 0
	v_add_u32_e32 v133, 0x4000, v132
	v_add_u32_e32 v134, 0x8000, v132
	v_add_u32_e32 v135, 0xc000, v132
	v_mfma_f32_16x16x32_bf16 v[74:77], v[148:151], v[70:73], 0
	v_add_u32_e32 v136, 0x10000, v132
	s_nop 2
	v_exp_f32_e32 v66, v66
	v_exp_f32_e32 v67, v67
	v_mfma_f32_16x16x32_bf16 v[78:81], v[152:155], v[70:73], 0
	v_exp_f32_e32 v68, v68
	v_exp_f32_e32 v69, v69
	v_exp_f32_e32 v74, v74
	v_mfma_f32_16x16x32_bf16 v[82:85], v[156:159], v[70:73], 0
	v_exp_f32_e32 v75, v75
	v_exp_f32_e32 v76, v76
	v_exp_f32_e32 v77, v77
	v_mfma_f32_16x16x32_bf16 v[86:89], v[160:163], v[70:73], 0
	v_exp_f32_e32 v78, v78
	v_exp_f32_e32 v79, v79
	v_exp_f32_e32 v80, v80
	v_mfma_f32_16x16x32_bf16 v[90:93], v[164:167], v[70:73], 0
	v_exp_f32_e32 v81, v81
	v_exp_f32_e32 v82, v82
	v_exp_f32_e32 v83, v83
	v_mfma_f32_16x16x32_bf16 v[94:97], v[168:171], v[70:73], 0
	v_exp_f32_e32 v84, v84
	v_exp_f32_e32 v85, v85
	v_exp_f32_e32 v86, v86
	v_mfma_f32_16x16x32_bf16 v[98:101], v[172:175], v[70:73], 0
	v_exp_f32_e32 v87, v87
	v_exp_f32_e32 v88, v88
	v_exp_f32_e32 v89, v89
	v_mfma_f32_16x16x32_bf16 v[102:105], v[176:179], v[70:73], 0
	v_exp_f32_e32 v90, v90
	v_exp_f32_e32 v91, v91
	v_exp_f32_e32 v92, v92
	v_mfma_f32_16x16x32_bf16 v[108:111], v[180:183], v[70:73], 0
	v_exp_f32_e32 v93, v93
	v_exp_f32_e32 v94, v94
	v_exp_f32_e32 v95, v95
	v_mfma_f32_16x16x32_bf16 v[112:115], v[184:187], v[70:73], 0
	v_exp_f32_e32 v96, v96
	v_exp_f32_e32 v97, v97
	v_exp_f32_e32 v98, v98
	v_mfma_f32_16x16x32_bf16 v[116:119], v[188:191], v[70:73], 0
	v_exp_f32_e32 v99, v99
	v_exp_f32_e32 v100, v100
	v_exp_f32_e32 v101, v101
	v_mfma_f32_16x16x32_bf16 v[120:123], v[232:235], v[70:73], 0
	v_exp_f32_e32 v102, v102
	v_exp_f32_e32 v103, v103
	v_exp_f32_e32 v104, v104
	v_mfma_f32_16x16x32_bf16 v[124:127], v[236:239], v[70:73], 0
	v_exp_f32_e32 v105, v105
	v_exp_f32_e32 v108, v108
	v_exp_f32_e32 v109, v109
	v_mfma_f32_16x16x32_bf16 v[128:131], v[240:243], v[70:73], 0
	v_exp_f32_e32 v110, v110
	v_exp_f32_e32 v111, v111
	v_exp_f32_e32 v112, v112
	v_mfma_f32_16x16x32_bf16 v[70:73], v[244:247], v[70:73], 0
	v_exp_f32_e32 v113, v113
	v_exp_f32_e32 v114, v114
	v_exp_f32_e32 v115, v115
	v_exp_f32_e32 v116, v116
	v_exp_f32_e32 v117, v117
	v_exp_f32_e32 v118, v118
	v_exp_f32_e32 v119, v119
	v_exp_f32_e32 v120, v120
	v_exp_f32_e32 v121, v121
	v_exp_f32_e32 v122, v122
	v_exp_f32_e32 v123, v123
	v_exp_f32_e32 v124, v124
	v_exp_f32_e32 v125, v125
	v_exp_f32_e32 v126, v126
	v_exp_f32_e32 v127, v127
	v_exp_f32_e32 v128, v128
	v_exp_f32_e32 v129, v129
	v_exp_f32_e32 v130, v130
	v_exp_f32_e32 v131, v131
	v_exp_f32_e32 v70, v70
	v_exp_f32_e32 v71, v71
	v_exp_f32_e32 v72, v72
	v_exp_f32_e32 v73, v73
	v_pk_add_f32 v[66:67], v[66:67], 1.0 op_sel_hi:[1,0]
	v_pk_add_f32 v[68:69], v[68:69], 1.0 op_sel_hi:[1,0]
	v_pk_add_f32 v[74:75], v[74:75], 1.0 op_sel_hi:[1,0]
	v_pk_add_f32 v[76:77], v[76:77], 1.0 op_sel_hi:[1,0]
	v_pk_add_f32 v[78:79], v[78:79], 1.0 op_sel_hi:[1,0]
	v_pk_add_f32 v[80:81], v[80:81], 1.0 op_sel_hi:[1,0]
	v_pk_add_f32 v[82:83], v[82:83], 1.0 op_sel_hi:[1,0]
	v_pk_add_f32 v[84:85], v[84:85], 1.0 op_sel_hi:[1,0]
	v_pk_add_f32 v[86:87], v[86:87], 1.0 op_sel_hi:[1,0]
	v_pk_add_f32 v[88:89], v[88:89], 1.0 op_sel_hi:[1,0]
	v_pk_add_f32 v[90:91], v[90:91], 1.0 op_sel_hi:[1,0]
	v_pk_add_f32 v[92:93], v[92:93], 1.0 op_sel_hi:[1,0]
	v_pk_add_f32 v[94:95], v[94:95], 1.0 op_sel_hi:[1,0]
	v_pk_add_f32 v[96:97], v[96:97], 1.0 op_sel_hi:[1,0]
	v_pk_add_f32 v[98:99], v[98:99], 1.0 op_sel_hi:[1,0]
	v_pk_add_f32 v[100:101], v[100:101], 1.0 op_sel_hi:[1,0]
	v_pk_add_f32 v[102:103], v[102:103], 1.0 op_sel_hi:[1,0]
	v_pk_add_f32 v[104:105], v[104:105], 1.0 op_sel_hi:[1,0]
	v_rcp_f32_e32 v66, v66
	v_rcp_f32_e32 v67, v67
	v_rcp_f32_e32 v68, v68
	v_rcp_f32_e32 v69, v69
	v_pk_add_f32 v[108:109], v[108:109], 1.0 op_sel_hi:[1,0]
	v_pk_add_f32 v[110:111], v[110:111], 1.0 op_sel_hi:[1,0]
	v_pk_add_f32 v[112:113], v[112:113], 1.0 op_sel_hi:[1,0]
	v_pk_add_f32 v[114:115], v[114:115], 1.0 op_sel_hi:[1,0]
	v_pk_add_f32 v[116:117], v[116:117], 1.0 op_sel_hi:[1,0]
	v_pk_add_f32 v[118:119], v[118:119], 1.0 op_sel_hi:[1,0]
	v_pk_add_f32 v[120:121], v[120:121], 1.0 op_sel_hi:[1,0]
	v_pk_add_f32 v[122:123], v[122:123], 1.0 op_sel_hi:[1,0]
	v_pk_add_f32 v[124:125], v[124:125], 1.0 op_sel_hi:[1,0]
	v_pk_add_f32 v[126:127], v[126:127], 1.0 op_sel_hi:[1,0]
	v_pk_add_f32 v[128:129], v[128:129], 1.0 op_sel_hi:[1,0]
	v_pk_add_f32 v[130:131], v[130:131], 1.0 op_sel_hi:[1,0]
	v_add_f32_e32 v140, 1.0, v70
	v_add_f32_e32 v141, 1.0, v71
	v_add_f32_e32 v142, 1.0, v72
	v_add_f32_e32 v143, 1.0, v73
	v_rcp_f32_e32 v70, v74
	v_rcp_f32_e32 v71, v75
	v_rcp_f32_e32 v72, v76
	v_rcp_f32_e32 v73, v77
	v_rcp_f32_e32 v74, v78
	v_rcp_f32_e32 v75, v79
	v_rcp_f32_e32 v76, v80
	v_rcp_f32_e32 v77, v81
	v_rcp_f32_e32 v78, v82
	v_rcp_f32_e32 v79, v83
	v_rcp_f32_e32 v80, v84
	v_rcp_f32_e32 v81, v85
	v_rcp_f32_e32 v82, v86
	v_rcp_f32_e32 v83, v87
	v_rcp_f32_e32 v84, v88
	v_rcp_f32_e32 v85, v89
	v_rcp_f32_e32 v86, v90
	v_rcp_f32_e32 v87, v91
	v_rcp_f32_e32 v88, v92
	v_rcp_f32_e32 v89, v93
	v_rcp_f32_e32 v90, v94
	v_rcp_f32_e32 v91, v95
	v_rcp_f32_e32 v92, v96
	v_rcp_f32_e32 v93, v97
	v_rcp_f32_e32 v94, v98
	v_rcp_f32_e32 v95, v99
	v_rcp_f32_e32 v96, v100
	v_rcp_f32_e32 v97, v101
	v_rcp_f32_e32 v98, v102
	v_rcp_f32_e32 v99, v103
	v_rcp_f32_e32 v100, v104
	v_rcp_f32_e32 v101, v105
	v_rcp_f32_e32 v102, v108
	v_rcp_f32_e32 v103, v109
	v_rcp_f32_e32 v104, v110
	v_rcp_f32_e32 v105, v111
	v_rcp_f32_e32 v108, v112
	v_rcp_f32_e32 v109, v113
	v_rcp_f32_e32 v110, v114
	v_rcp_f32_e32 v111, v115
	v_rcp_f32_e32 v112, v116
	v_rcp_f32_e32 v113, v117
	v_rcp_f32_e32 v114, v118
	v_rcp_f32_e32 v115, v119
	v_rcp_f32_e32 v116, v120
	v_rcp_f32_e32 v117, v121
	v_rcp_f32_e32 v118, v122
	v_rcp_f32_e32 v119, v123
	v_rcp_f32_e32 v120, v124
	v_rcp_f32_e32 v121, v125
	v_rcp_f32_e32 v122, v126
	v_rcp_f32_e32 v123, v127
	v_rcp_f32_e32 v124, v128
	v_rcp_f32_e32 v125, v129
	v_rcp_f32_e32 v126, v130
	v_rcp_f32_e32 v127, v131
	v_rcp_f32_e32 v128, v140
	v_rcp_f32_e32 v129, v141
	v_rcp_f32_e32 v130, v142
	v_rcp_f32_e32 v131, v143
	v_pk_fma_f32 v[66:67], v[66:67], -2.0, 1.0 op_sel_hi:[1,0,0]
	v_pk_fma_f32 v[68:69], v[68:69], -2.0, 1.0 op_sel_hi:[1,0,0]
	v_pk_fma_f32 v[70:71], v[70:71], -2.0, 1.0 op_sel_hi:[1,0,0]
	v_pk_fma_f32 v[72:73], v[72:73], -2.0, 1.0 op_sel_hi:[1,0,0]
	v_pk_fma_f32 v[74:75], v[74:75], -2.0, 1.0 op_sel_hi:[1,0,0]
	v_pk_fma_f32 v[76:77], v[76:77], -2.0, 1.0 op_sel_hi:[1,0,0]
	v_pk_fma_f32 v[78:79], v[78:79], -2.0, 1.0 op_sel_hi:[1,0,0]
	v_pk_fma_f32 v[80:81], v[80:81], -2.0, 1.0 op_sel_hi:[1,0,0]
	v_pk_fma_f32 v[82:83], v[82:83], -2.0, 1.0 op_sel_hi:[1,0,0]
	v_pk_fma_f32 v[84:85], v[84:85], -2.0, 1.0 op_sel_hi:[1,0,0]
	v_pk_fma_f32 v[86:87], v[86:87], -2.0, 1.0 op_sel_hi:[1,0,0]
	v_pk_fma_f32 v[88:89], v[88:89], -2.0, 1.0 op_sel_hi:[1,0,0]
	v_pk_fma_f32 v[90:91], v[90:91], -2.0, 1.0 op_sel_hi:[1,0,0]
	v_pk_fma_f32 v[92:93], v[92:93], -2.0, 1.0 op_sel_hi:[1,0,0]
	v_pk_fma_f32 v[94:95], v[94:95], -2.0, 1.0 op_sel_hi:[1,0,0]
	v_pk_fma_f32 v[96:97], v[96:97], -2.0, 1.0 op_sel_hi:[1,0,0]
	v_pk_fma_f32 v[98:99], v[98:99], -2.0, 1.0 op_sel_hi:[1,0,0]
	v_pk_fma_f32 v[100:101], v[100:101], -2.0, 1.0 op_sel_hi:[1,0,0]
	ds_write_b128 v214, v[66:69]
	ds_write_b128 v214, v[70:73] offset:64
	ds_write_b128 v214, v[74:77] offset:128
	ds_write_b128 v214, v[78:81] offset:192
	ds_write_b128 v214, v[82:85] offset:256
	ds_write_b128 v214, v[86:89] offset:320
	ds_write_b128 v214, v[90:93] offset:384
	ds_write_b128 v214, v[94:97] offset:448
	v_pk_fma_f32 v[102:103], v[102:103], -2.0, 1.0 op_sel_hi:[1,0,0]
	v_pk_fma_f32 v[104:105], v[104:105], -2.0, 1.0 op_sel_hi:[1,0,0]
	v_pk_fma_f32 v[108:109], v[108:109], -2.0, 1.0 op_sel_hi:[1,0,0]
	v_pk_fma_f32 v[110:111], v[110:111], -2.0, 1.0 op_sel_hi:[1,0,0]
	v_pk_fma_f32 v[112:113], v[112:113], -2.0, 1.0 op_sel_hi:[1,0,0]
	v_pk_fma_f32 v[114:115], v[114:115], -2.0, 1.0 op_sel_hi:[1,0,0]
	v_pk_fma_f32 v[116:117], v[116:117], -2.0, 1.0 op_sel_hi:[1,0,0]
	v_pk_fma_f32 v[118:119], v[118:119], -2.0, 1.0 op_sel_hi:[1,0,0]
	v_pk_fma_f32 v[120:121], v[120:121], -2.0, 1.0 op_sel_hi:[1,0,0]
	v_pk_fma_f32 v[122:123], v[122:123], -2.0, 1.0 op_sel_hi:[1,0,0]
	v_pk_fma_f32 v[124:125], v[124:125], -2.0, 1.0 op_sel_hi:[1,0,0]
	v_pk_fma_f32 v[126:127], v[126:127], -2.0, 1.0 op_sel_hi:[1,0,0]
	v_pk_fma_f32 v[128:129], v[128:129], -2.0, 1.0 op_sel_hi:[1,0,0]
	v_pk_fma_f32 v[130:131], v[130:131], -2.0, 1.0 op_sel_hi:[1,0,0]
	ds_read_b128 v[66:69], v215
	ds_read_b128 v[70:73], v215 offset:1056
	ds_read_b128 v[74:77], v215 offset:2112
	ds_read_b128 v[78:81], v215 offset:3168
	ds_read_b128 v[82:85], v215 offset:4224
	ds_read_b128 v[86:89], v215 offset:5280
	ds_read_b128 v[90:93], v215 offset:6336
	ds_read_b128 v[94:97], v215 offset:7392
	ds_write_b128 v214, v[98:101]
	ds_write_b128 v214, v[102:105] offset:64
	ds_write_b128 v214, v[108:111] offset:128
	ds_write_b128 v214, v[112:115] offset:192
	ds_write_b128 v214, v[116:119] offset:256
	ds_write_b128 v214, v[120:123] offset:320
	ds_write_b128 v214, v[124:127] offset:384
	ds_write_b128 v214, v[128:131] offset:448
	ds_read_b128 v[98:101], v215
	ds_read_b128 v[102:105], v215 offset:1056
	ds_read_b128 v[108:111], v215 offset:2112
	ds_read_b128 v[112:115], v215 offset:3168
	ds_read_b128 v[116:119], v215 offset:4224
	ds_read_b128 v[120:123], v215 offset:5280
	ds_read_b128 v[124:127], v215 offset:6336
	ds_read_b128 v[128:131], v215 offset:7392
	v_add_u32_e32 v137, 0x14000, v132
	v_add_u32_e32 v138, 0x18000, v132
	v_add_u32_e32 v139, 0x1c000, v132
	s_waitcnt lgkmcnt(14)
	buffer_store_dwordx4 v[66:69], v132, s[8:11], 0 offen sc0 nt sc1
	buffer_store_dwordx4 v[70:73], v133, s[8:11], 0 offen sc0 nt sc1
	buffer_store_dwordx4 v[74:77], v134, s[8:11], 0 offen sc0 nt sc1
	buffer_store_dwordx4 v[78:81], v135, s[8:11], 0 offen sc0 nt sc1
	buffer_store_dwordx4 v[82:85], v136, s[8:11], 0 offen sc0 nt sc1
	buffer_store_dwordx4 v[86:89], v137, s[8:11], 0 offen sc0 nt sc1
	buffer_store_dwordx4 v[90:93], v138, s[8:11], 0 offen sc0 nt sc1
	buffer_store_dwordx4 v[94:97], v139, s[8:11], 0 offen sc0 nt sc1
	s_waitcnt lgkmcnt(7)
	buffer_store_dwordx4 v[98:101], v132, s[8:11], 0 offen offset:512 sc0 nt sc1
	s_waitcnt lgkmcnt(6)
	buffer_store_dwordx4 v[102:105], v133, s[8:11], 0 offen offset:512 sc0 nt sc1
	s_waitcnt lgkmcnt(5)
	buffer_store_dwordx4 v[108:111], v134, s[8:11], 0 offen offset:512 sc0 nt sc1
	s_waitcnt lgkmcnt(4)
	buffer_store_dwordx4 v[112:115], v135, s[8:11], 0 offen offset:512 sc0 nt sc1
	s_waitcnt lgkmcnt(3)
	buffer_store_dwordx4 v[116:119], v136, s[8:11], 0 offen offset:512 sc0 nt sc1
	s_waitcnt lgkmcnt(2)
	buffer_store_dwordx4 v[120:123], v137, s[8:11], 0 offen offset:512 sc0 nt sc1
	s_waitcnt lgkmcnt(1)
	buffer_store_dwordx4 v[124:127], v138, s[8:11], 0 offen offset:512 sc0 nt sc1
	s_waitcnt lgkmcnt(0)
	buffer_store_dwordx4 v[128:131], v139, s[8:11], 0 offen offset:512 sc0 nt sc1
	s_cbranch_scc0 .LBB0_3
	s_endpgm
